# v49 + both G1 (mixer in-projection) epilogues rewritten by hand: rstd8 via DPP quad sums, SS loads issued before the epilogue-alignment barrier, one-block-deep pipelined bpermute/store; bit-identical
# speedup vs baseline: 1.0177x; 1.0011x over previous
; #define PG8_STAGE_A(b, h, ptr, NX) do { if constexpr (Sched::GATHER) { unsigned gs_[2]; gs_[0] = ((NX) && last_) ? gN[h][0] : gA[h][0]; gs_[1] = ((NX) && last_) ? gN[h][1] : gA[h][1]; PG8_STAGE(PG8_SA(b, h), ptr, gs_); } \
;         else PG8_STAGE(PG8_SA(b, h), (ptr) + ((h) ? hstep : (size_t)0), voffA); } while (0)
; #define PG8_STAGE(bufoff, gbase, voff) do { _Pragma("unroll") for (int _i = 0; _i < 2; ++_i) \
;         __builtin_amdgcn_global_load_lds((const unsigned*)((const char*)(gbase) + (voff)[_i]), (PG8_LAS unsigned*)(lds + (bufoff) + ldsw + _i * 8192), 16, 0, 0); } while (0)
; #define PG8_WAIT_V(n) asm volatile("s_waitcnt vmcnt(" #n ")" ::: "memory")
; #define PG8_BAR __builtin_amdgcn_s_barrier()
; template <class Epi, class Sched, bool ALIGN_EPI = false, bool SP2 = false>
; __device__ __forceinline__ void gemm_phase(PG8_LAS unsigned char* lds, const Gemm g, const Sched& S, const Epi& E, const bool skip_epi = false) {
;     ...
;         for (int t = 0; t < nt; t += 2) {
;             const bool last = (t == nt - 2); last_ = last && has_next;
;             const char* a1 = cA + (size_t)(t + 1) * kstep;
;             const char* a2 = last ? nA : cA + (size_t)(t + 2) * kstep; const char* b2 = last ? nB : cB + (size_t)(t + 2) * kstep;
;             const char* a3 = a2 + kstep; const char* b3 = b2 + kstep;
;             if (last && has_next) S.a_ready(nxt);
;             if constexpr (SP2) {
;             PG8_LDB(B0, 0, 0); PG8_LDB(B1, 0, 1); PG8_SCHED; PG8_LDA(At, 0, 0); PG8_STAGE_A(1, 1, a1, false);
;             PG8_WAIT_V(8); PG8_WAIT_L(0); PG8_BAR; PG8_MMA(0, 0, At, B0); PG8_MMA(0, 1, At, B1); PG8_BAR; PG8_SCHED;
;             PG8_LDA(At, 0, 1); PG8_STAGE(PG8_SB(0, 0), b2, voffB); PG8_STAGE(PG8_SB(0, 1), b2 + hstep, voffB); PG8_STAGE_A(0, 0, a2, true);
;             PG8_WAIT_V(8); PG8_WAIT_L(0); PG8_BAR; PG8_MMA(1, 0, At, B0); PG8_MMA(1, 1, At, B1); PG8_BAR; PG8_SCHED;
;             PG8_LDB(B0, 1, 0); PG8_LDB(B1, 1, 1); PG8_SCHED; PG8_LDA(At, 1, 0); PG8_STAGE_A(0, 1, a2, true);
;             PG8_WAIT_V(8); PG8_WAIT_L(0); PG8_BAR; PG8_MMA(0, 0, At, B0); PG8_MMA(0, 1, At, B1); PG8_BAR; PG8_SCHED;
;             PG8_LDA(At, 1, 1); PG8_STAGE(PG8_SB(1, 0), b3, voffB); PG8_STAGE(PG8_SB(1, 1), b3 + hstep, voffB); PG8_STAGE_A(1, 0, a3, true);
;             PG8_WAIT_V(8); PG8_WAIT_L(0); PG8_BAR; PG8_MMA(1, 0, At, B0); PG8_MMA(1, 1, At, B1); PG8_BAR; PG8_SCHED;
.LBB0_253:
	ds_read_b128 v[148:151], v170
	ds_read_b128 v[152:155], v170 offset:1024
	ds_read_b128 v[156:159], v170 offset:2048
	ds_read_b128 v[160:163], v170 offset:3072
	ds_read_b128 v[176:179], v171
	ds_read_b128 v[180:183], v171 offset:1024
	ds_read_b128 v[184:187], v171 offset:2048
	ds_read_b128 v[188:191], v171 offset:3072
	s_add_u32 s26, s24, 0xfffc0080
	s_addc_u32 s27, s25, -1
	s_cmp_eq_u32 s60, 12
	s_cselect_b32 s29, s17, s27
	s_cselect_b32 s28, s56, s26
	s_cselect_b32 s27, s15, s59
	s_cselect_b32 s26, s57, s58
	v_lshl_add_u64 v[164:165], s[24:25], 0, v[140:141]
	s_add_i32 m0, s23, 0xc000
	ds_read_b128 v[192:195], v172
	ds_read_b128 v[196:199], v172 offset:1024
	ds_read_b128 v[200:203], v172 offset:2048
	ds_read_b128 v[204:207], v172 offset:3072
	ds_read_b128 v[208:211], v172 offset:4096
	ds_read_b128 v[212:215], v172 offset:5120
	ds_read_b128 v[216:219], v172 offset:6144
	ds_read_b128 v[220:223], v172 offset:7168
	global_load_lds_dwordx4 v[164:165], off
	v_lshl_add_u64 v[164:165], s[24:25], 0, v[142:143]
	s_add_i32 m0, s23, 0xe000
	s_nop 0
	global_load_lds_dwordx4 v[164:165], off
	s_waitcnt vmcnt(8)
	s_waitcnt lgkmcnt(0)
	s_barrier
	s_setprio 1
	s_waitcnt lgkmcnt(0)
	v_mfma_f32_16x16x32_bf16 v[126:129], v[148:151], v[192:195], v[126:129]
	v_mfma_f32_16x16x32_bf16 v[122:125], v[156:159], v[192:195], v[122:125]
	v_mfma_f32_16x16x32_bf16 v[114:117], v[148:151], v[200:203], v[114:117]
	v_mfma_f32_16x16x32_bf16 v[106:109], v[156:159], v[200:203], v[106:109]
	v_mfma_f32_16x16x32_bf16 v[98:101], v[148:151], v[208:211], v[98:101]
	v_mfma_f32_16x16x32_bf16 v[90:93], v[156:159], v[208:211], v[90:93]
	v_mfma_f32_16x16x32_bf16 v[82:85], v[148:151], v[216:219], v[82:85]
	v_mfma_f32_16x16x32_bf16 v[74:77], v[156:159], v[216:219], v[74:77]
	v_mfma_f32_16x16x32_bf16 v[126:129], v[152:155], v[196:199], v[126:129]
	v_mfma_f32_16x16x32_bf16 v[122:125], v[160:163], v[196:199], v[122:125]
	v_mfma_f32_16x16x32_bf16 v[114:117], v[152:155], v[204:207], v[114:117]
	v_mfma_f32_16x16x32_bf16 v[106:109], v[160:163], v[204:207], v[106:109]
	v_mfma_f32_16x16x32_bf16 v[98:101], v[152:155], v[212:215], v[98:101]
	v_mfma_f32_16x16x32_bf16 v[90:93], v[160:163], v[212:215], v[90:93]
	v_mfma_f32_16x16x32_bf16 v[82:85], v[152:155], v[220:223], v[82:85]
	v_mfma_f32_16x16x32_bf16 v[74:77], v[160:163], v[220:223], v[74:77]
	s_setprio 0
	s_setprio 1
	v_mfma_f32_16x16x32_bf16 v[118:121], v[176:179], v[192:195], v[118:121]
	v_mfma_f32_16x16x32_bf16 v[110:113], v[184:187], v[192:195], v[110:113]
	v_mfma_f32_16x16x32_bf16 v[102:105], v[176:179], v[200:203], v[102:105]
	v_mfma_f32_16x16x32_bf16 v[94:97], v[184:187], v[200:203], v[94:97]
	v_mfma_f32_16x16x32_bf16 v[86:89], v[176:179], v[208:211], v[86:89]
	v_mfma_f32_16x16x32_bf16 v[78:81], v[184:187], v[208:211], v[78:81]
	v_mfma_f32_16x16x32_bf16 v[70:73], v[176:179], v[216:219], v[70:73]
	v_mfma_f32_16x16x32_bf16 v[66:69], v[184:187], v[216:219], v[66:69]
	v_mfma_f32_16x16x32_bf16 v[118:121], v[180:183], v[196:199], v[118:121]
	v_mfma_f32_16x16x32_bf16 v[110:113], v[188:191], v[196:199], v[110:113]
	v_mfma_f32_16x16x32_bf16 v[102:105], v[180:183], v[204:207], v[102:105]
	v_mfma_f32_16x16x32_bf16 v[94:97], v[188:191], v[204:207], v[94:97]
	v_mfma_f32_16x16x32_bf16 v[86:89], v[180:183], v[212:215], v[86:89]
	v_mfma_f32_16x16x32_bf16 v[78:81], v[188:191], v[212:215], v[78:81]
	v_mfma_f32_16x16x32_bf16 v[70:73], v[180:183], v[220:223], v[70:73]
	v_mfma_f32_16x16x32_bf16 v[66:69], v[188:191], v[220:223], v[66:69]
	s_setprio 0
	s_barrier
	s_add_i32 s61, s46, s2
	v_lshl_add_u64 v[164:165], s[26:27], 0, v[134:135]
	s_mov_b32 m0, s61
	ds_read_b128 v[192:195], v172 offset:16384
	ds_read_b128 v[196:199], v172 offset:17408
	ds_read_b128 v[200:203], v172 offset:18432
	ds_read_b128 v[204:207], v172 offset:19456
	ds_read_b128 v[208:211], v172 offset:20480
	ds_read_b128 v[212:215], v172 offset:21504
	ds_read_b128 v[216:219], v172 offset:22528
	ds_read_b128 v[220:223], v172 offset:23552
	global_load_lds_dwordx4 v[164:165], off
	s_add_i32 m0, s61, 0x2000
	s_add_u32 s62, s26, 0x40000
	v_lshl_add_u64 v[224:225], s[26:27], 0, v[130:131]
	s_addc_u32 s63, s27, 0
	s_add_i32 s61, s47, s2
	global_load_lds_dwordx4 v[224:225], off
	v_lshl_add_u64 v[226:227], s[62:63], 0, v[134:135]
	s_mov_b32 m0, s61
	v_lshl_add_u64 v[230:231], s[28:29], 0, v[132:133]
	global_load_lds_dwordx4 v[226:227], off
	v_lshl_add_u64 v[226:227], s[62:63], 0, v[130:131]
	s_add_i32 m0, s61, 0x2000
	s_nop 0
	global_load_lds_dwordx4 v[226:227], off
	v_lshl_add_u64 v[226:227], s[28:29], 0, v[136:137]
	s_mov_b32 m0, s23
	s_nop 0
	global_load_lds_dwordx4 v[226:227], off
	s_mov_b32 m0, s31
	s_nop 0
	global_load_lds_dwordx4 v[230:231], off
	s_waitcnt vmcnt(8)
	s_waitcnt lgkmcnt(0)
	s_barrier
; #define PG8_STAGE_A(b, h, ptr, NX) do { if constexpr (Sched::GATHER) { unsigned gs_[2]; gs_[0] = ((NX) && last_) ? gN[h][0] : gA[h][0]; gs_[1] = ((NX) && last_) ? gN[h][1] : gA[h][1]; PG8_STAGE(PG8_SA(b, h), ptr, gs_); } \
;         else PG8_STAGE(PG8_SA(b, h), (ptr) + ((h) ? hstep : (size_t)0), voffA); } while (0)
; #define PG8_STAGE(bufoff, gbase, voff) do { _Pragma("unroll") for (int _i = 0; _i < 2; ++_i) \
;         __builtin_amdgcn_global_load_lds((const unsigned*)((const char*)(gbase) + (voff)[_i]), (PG8_LAS unsigned*)(lds + (bufoff) + ldsw + _i * 8192), 16, 0, 0); } while (0)
; #define PG8_LDA(dst, b, h) do { _Pragma("unroll") for (int m = 0; m < 4; ++m) _Pragma("unroll") for (int k = 0; k < 2; ++k) dst[m][k] = *(const PG8_LAS bf16x8*)(lds + PG8_SA(b, h) + aoff + m * 2048 + k * 1024); } while (0)
; #define PG8_LDB(dst, b, h) do { _Pragma("unroll") for (int n = 0; n < 2; ++n) _Pragma("unroll") for (int k = 0; k < 2; ++k) dst[n][k] = *(const PG8_LAS bf16x8*)(lds + PG8_SB(b, h) + boff + n * 2048 + k * 1024); } while (0)
; #define PG8_MMA(ai, bj, At, Bt) do { __builtin_amdgcn_s_setprio(1); _Pragma("unroll") for (int m = 0; m < 4; ++m) _Pragma("unroll") for (int n = 0; n < 2; ++n) _Pragma("unroll") for (int k = 0; k < 2; ++k) \
;         acc[ai][bj][m][n] = __builtin_amdgcn_mfma_f32_16x16x32_bf16(Bt[n][k], At[m][k], acc[ai][bj][m][n], 0, 0, 0); __builtin_amdgcn_s_setprio(0); } while (0)
; template <class Epi, class Sched, bool ALIGN_EPI = false, bool SP2 = false>
; __device__ __forceinline__ void gemm_phase(PG8_LAS unsigned char* lds, const Gemm g, const Sched& S, const Epi& E, const bool skip_epi = false) {
;     ...
;             PG8_WAIT_V(8); PG8_WAIT_L(0); PG8_BAR; PG8_MMA(0, 0, At, B0); PG8_MMA(0, 1, At, B1); PG8_BAR; PG8_SCHED;
;             PG8_LDA(At, 0, 1); PG8_STAGE(PG8_SB(0, 0), b2, voffB); PG8_STAGE(PG8_SB(0, 1), b2 + hstep, voffB); PG8_STAGE_A(0, 0, a2, true);
;             PG8_WAIT_V(8); PG8_WAIT_L(0); PG8_BAR; PG8_MMA(1, 0, At, B0); PG8_MMA(1, 1, At, B1); PG8_BAR; PG8_SCHED;
;             PG8_LDB(B0, 1, 0); PG8_LDB(B1, 1, 1); PG8_SCHED; PG8_LDA(At, 1, 0); PG8_STAGE_A(0, 1, a2, true);
;             PG8_WAIT_V(8); PG8_WAIT_L(0); PG8_BAR; PG8_MMA(0, 0, At, B0); PG8_MMA(0, 1, At, B1); PG8_BAR; PG8_SCHED;
;             PG8_LDA(At, 1, 1); PG8_STAGE(PG8_SB(1, 0), b3, voffB); PG8_STAGE(PG8_SB(1, 1), b3 + hstep, voffB); PG8_STAGE_A(1, 0, a3, true);
	s_setprio 1
	s_waitcnt lgkmcnt(0)
	v_mfma_f32_16x16x32_bf16 v[62:65], v[148:151], v[192:195], v[62:65]
	v_mfma_f32_16x16x32_bf16 v[58:61], v[156:159], v[192:195], v[58:61]
	v_mfma_f32_16x16x32_bf16 v[50:53], v[148:151], v[200:203], v[50:53]
	v_mfma_f32_16x16x32_bf16 v[42:45], v[156:159], v[200:203], v[42:45]
	v_mfma_f32_16x16x32_bf16 v[34:37], v[148:151], v[208:211], v[34:37]
	v_mfma_f32_16x16x32_bf16 v[26:29], v[156:159], v[208:211], v[26:29]
	v_mfma_f32_16x16x32_bf16 v[18:21], v[148:151], v[216:219], v[18:21]
	v_mfma_f32_16x16x32_bf16 v[10:13], v[156:159], v[216:219], v[10:13]
	v_mfma_f32_16x16x32_bf16 v[62:65], v[152:155], v[196:199], v[62:65]
	v_mfma_f32_16x16x32_bf16 v[58:61], v[160:163], v[196:199], v[58:61]
	v_mfma_f32_16x16x32_bf16 v[50:53], v[152:155], v[204:207], v[50:53]
	v_mfma_f32_16x16x32_bf16 v[42:45], v[160:163], v[204:207], v[42:45]
	v_mfma_f32_16x16x32_bf16 v[34:37], v[152:155], v[212:215], v[34:37]
	v_mfma_f32_16x16x32_bf16 v[26:29], v[160:163], v[212:215], v[26:29]
	v_mfma_f32_16x16x32_bf16 v[18:21], v[152:155], v[220:223], v[18:21]
	v_mfma_f32_16x16x32_bf16 v[10:13], v[160:163], v[220:223], v[10:13]
	s_setprio 0
	s_setprio 1
	v_mfma_f32_16x16x32_bf16 v[54:57], v[176:179], v[192:195], v[54:57]
	v_mfma_f32_16x16x32_bf16 v[46:49], v[184:187], v[192:195], v[46:49]
	v_mfma_f32_16x16x32_bf16 v[38:41], v[176:179], v[200:203], v[38:41]
	v_mfma_f32_16x16x32_bf16 v[30:33], v[184:187], v[200:203], v[30:33]
	v_mfma_f32_16x16x32_bf16 v[22:25], v[176:179], v[208:211], v[22:25]
	v_mfma_f32_16x16x32_bf16 v[14:17], v[184:187], v[208:211], v[14:17]
	v_mfma_f32_16x16x32_bf16 v[6:9], v[176:179], v[216:219], v[6:9]
	v_mfma_f32_16x16x32_bf16 v[2:5], v[184:187], v[216:219], v[2:5]
	v_mfma_f32_16x16x32_bf16 v[54:57], v[180:183], v[196:199], v[54:57]
	v_mfma_f32_16x16x32_bf16 v[46:49], v[188:191], v[196:199], v[46:49]
	v_mfma_f32_16x16x32_bf16 v[38:41], v[180:183], v[204:207], v[38:41]
	v_mfma_f32_16x16x32_bf16 v[30:33], v[188:191], v[204:207], v[30:33]
	v_mfma_f32_16x16x32_bf16 v[22:25], v[180:183], v[212:215], v[22:25]
	v_mfma_f32_16x16x32_bf16 v[14:17], v[188:191], v[212:215], v[14:17]
	v_mfma_f32_16x16x32_bf16 v[6:9], v[180:183], v[220:223], v[6:9]
	v_mfma_f32_16x16x32_bf16 v[2:5], v[188:191], v[220:223], v[2:5]
	s_setprio 0
	s_barrier
	s_add_i32 s61, 0, 0x18000
	s_add_i32 s62, 0, 0x1c000
	v_add_u32_e32 v160, s61, v1
	v_add_u32_e32 v188, s62, v1
	ds_read_b128 v[148:151], v160
	ds_read_b128 v[152:155], v160 offset:1024
	ds_read_b128 v[156:159], v160 offset:2048
	ds_read_b128 v[160:163], v160 offset:3072
	ds_read_b128 v[176:179], v188
	ds_read_b128 v[180:183], v188 offset:1024
	ds_read_b128 v[184:187], v188 offset:2048
	ds_read_b128 v[188:191], v188 offset:3072
	s_add_u32 s28, s28, 0x40000
	s_addc_u32 s29, s29, 0
	s_mov_b32 m0, s34
	v_lshl_add_u64 v[232:233], s[28:29], 0, v[136:137]
	ds_read_b128 v[192:195], v172 offset:32768
	ds_read_b128 v[196:199], v172 offset:33792
	ds_read_b128 v[200:203], v172 offset:34816
	ds_read_b128 v[204:207], v172 offset:35840
	ds_read_b128 v[208:211], v172 offset:36864
	ds_read_b128 v[212:215], v172 offset:37888
	ds_read_b128 v[216:219], v172 offset:38912
	ds_read_b128 v[220:223], v172 offset:39936
	global_load_lds_dwordx4 v[232:233], off
	v_lshl_add_u64 v[232:233], s[28:29], 0, v[132:133]
	s_mov_b32 m0, s35
	s_nop 0
	global_load_lds_dwordx4 v[232:233], off
	s_waitcnt vmcnt(8)
	s_waitcnt lgkmcnt(0)
	s_barrier
	s_setprio 1
	s_waitcnt lgkmcnt(0)
	v_mfma_f32_16x16x32_bf16 v[126:129], v[148:151], v[192:195], v[126:129]
	v_mfma_f32_16x16x32_bf16 v[122:125], v[156:159], v[192:195], v[122:125]
	v_mfma_f32_16x16x32_bf16 v[114:117], v[148:151], v[200:203], v[114:117]
	v_mfma_f32_16x16x32_bf16 v[106:109], v[156:159], v[200:203], v[106:109]
	v_mfma_f32_16x16x32_bf16 v[98:101], v[148:151], v[208:211], v[98:101]
	v_mfma_f32_16x16x32_bf16 v[90:93], v[156:159], v[208:211], v[90:93]
	v_mfma_f32_16x16x32_bf16 v[82:85], v[148:151], v[216:219], v[82:85]
	v_mfma_f32_16x16x32_bf16 v[74:77], v[156:159], v[216:219], v[74:77]
	v_mfma_f32_16x16x32_bf16 v[126:129], v[152:155], v[196:199], v[126:129]
	v_mfma_f32_16x16x32_bf16 v[122:125], v[160:163], v[196:199], v[122:125]
	v_mfma_f32_16x16x32_bf16 v[114:117], v[152:155], v[204:207], v[114:117]
	v_mfma_f32_16x16x32_bf16 v[106:109], v[160:163], v[204:207], v[106:109]
	v_mfma_f32_16x16x32_bf16 v[98:101], v[152:155], v[212:215], v[98:101]
	v_mfma_f32_16x16x32_bf16 v[90:93], v[160:163], v[212:215], v[90:93]
	v_mfma_f32_16x16x32_bf16 v[82:85], v[152:155], v[220:223], v[82:85]
	v_mfma_f32_16x16x32_bf16 v[74:77], v[160:163], v[220:223], v[74:77]
	s_setprio 0
	s_setprio 1
	v_mfma_f32_16x16x32_bf16 v[118:121], v[176:179], v[192:195], v[118:121]
	v_mfma_f32_16x16x32_bf16 v[110:113], v[184:187], v[192:195], v[110:113]
	v_mfma_f32_16x16x32_bf16 v[102:105], v[176:179], v[200:203], v[102:105]
	v_mfma_f32_16x16x32_bf16 v[94:97], v[184:187], v[200:203], v[94:97]
	v_mfma_f32_16x16x32_bf16 v[86:89], v[176:179], v[208:211], v[86:89]
	v_mfma_f32_16x16x32_bf16 v[78:81], v[184:187], v[208:211], v[78:81]
	v_mfma_f32_16x16x32_bf16 v[70:73], v[176:179], v[216:219], v[70:73]
	v_mfma_f32_16x16x32_bf16 v[66:69], v[184:187], v[216:219], v[66:69]
	v_mfma_f32_16x16x32_bf16 v[118:121], v[180:183], v[196:199], v[118:121]
	v_mfma_f32_16x16x32_bf16 v[110:113], v[188:191], v[196:199], v[110:113]
	v_mfma_f32_16x16x32_bf16 v[102:105], v[180:183], v[204:207], v[102:105]
	v_mfma_f32_16x16x32_bf16 v[94:97], v[188:191], v[204:207], v[94:97]
	v_mfma_f32_16x16x32_bf16 v[86:89], v[180:183], v[212:215], v[86:89]
	v_mfma_f32_16x16x32_bf16 v[78:81], v[188:191], v[212:215], v[78:81]
	v_mfma_f32_16x16x32_bf16 v[70:73], v[180:183], v[220:223], v[70:73]
	v_mfma_f32_16x16x32_bf16 v[66:69], v[188:191], v[220:223], v[66:69]
	s_setprio 0
	s_barrier
; #define PG8_WAIT_V(n) asm volatile("s_waitcnt vmcnt(" #n ")" ::: "memory")
; #define PG8_BAR __builtin_amdgcn_s_barrier()
; __device__ __forceinline__ void rstd8(const float* SS, int rowb, int lane, float (&rs)[2][4]) {
;     f32x4 p[2][4];
; #pragma unroll
;     for (int ai = 0; ai < 2; ++ai)
; #pragma unroll
;         for (int m = 0; m < 4; ++m) p[ai][m] = *(const f32x4*)(SS + (size_t)(rowb + HALF * ai + 16 * m + (lane >> 2)) * 16 + 4 * (lane & 3));
;     asm volatile("" : "+v"(p[0][0]), "+v"(p[0][1]), "+v"(p[0][2]), "+v"(p[0][3]), "+v"(p[1][0]), "+v"(p[1][1]), "+v"(p[1][2]), "+v"(p[1][3]));
; template <class Epi, class Sched, bool ALIGN_EPI = false, bool SP2 = false>
; __device__ __forceinline__ void gemm_phase(PG8_LAS unsigned char* lds, const Gemm g, const Sched& S, const Epi& E, const bool skip_epi = false) {
;     ...
;             PG8_LDA(At, 1, 1); PG8_STAGE(PG8_SB(1, 0), b3, voffB); PG8_STAGE(PG8_SB(1, 1), b3 + hstep, voffB); PG8_STAGE_A(1, 0, a3, true);
;             PG8_WAIT_V(8); PG8_WAIT_L(0); PG8_BAR; PG8_MMA(1, 0, At, B0); PG8_MMA(1, 1, At, B1); PG8_BAR; PG8_SCHED;
;             } else {
;             PG8_LDB(B0, 0, 0); PG8_SCHED; PG8_LDA(At, 0, 0); PG8_STAGE_A(1, 1, a1, false);
;             PG8_WAIT_L(8); PG8_BAR; PG8_WAIT_L(0); PG8_MMA(0, 0, At, B0); PG8_BAR; PG8_SCHED;
;             PG8_LDB(B1, 0, 1); PG8_STAGE(PG8_SB(0, 0), b2, voffB);
;             PG8_BAR; PG8_WAIT_L(0); PG8_MMA(0, 1, At, B1); PG8_BAR;
;             PG8_LDA(At, 0, 1); PG8_STAGE_A(0, 0, a2, true);
;             PG8_BAR; PG8_WAIT_L(0); PG8_MMA(1, 0, At, B0); PG8_BAR; PG8_SCHED;
;             PG8_STAGE(PG8_SB(0, 1), b2 + hstep, voffB);
;             PG8_WAIT_V(6); PG8_BAR; PG8_MMA(1, 1, At, B1); PG8_BAR;
;             PG8_LDB(B0, 1, 0); PG8_SCHED; PG8_LDA(At, 1, 0); PG8_STAGE_A(0, 1, a2, true);
;             PG8_WAIT_L(8); PG8_BAR; PG8_WAIT_L(0); PG8_MMA(0, 0, At, B0); PG8_BAR; PG8_SCHED;
;             PG8_LDB(B1, 1, 1); PG8_STAGE(PG8_SB(1, 0), b3, voffB);
;             PG8_BAR; PG8_WAIT_L(0); PG8_MMA(0, 1, At, B1); PG8_BAR;
;             PG8_LDA(At, 1, 1); PG8_STAGE_A(1, 0, a3, true);
;             PG8_BAR; PG8_WAIT_L(0); PG8_MMA(1, 0, At, B0); PG8_BAR; PG8_SCHED;
;             PG8_STAGE(PG8_SB(1, 1), b3 + hstep, voffB);
;             PG8_WAIT_V(6); PG8_BAR; PG8_MMA(1, 1, At, B1); PG8_BAR;
;             }
;         }
;         if constexpr (ALIGN_EPI) { if (wr == 0) PG8_BAR; }
	s_add_i32 s28, s61, s2
	v_lshl_add_u64 v[164:165], v[164:165], 0, s[10:11]
	s_mov_b32 m0, s28
	ds_read_b128 v[192:195], v172 offset:49152
	ds_read_b128 v[196:199], v172 offset:50176
	ds_read_b128 v[200:203], v172 offset:51200
	ds_read_b128 v[204:207], v172 offset:52224
	ds_read_b128 v[208:211], v172 offset:53248
	ds_read_b128 v[212:215], v172 offset:54272
	ds_read_b128 v[216:219], v172 offset:55296
	ds_read_b128 v[220:223], v172 offset:56320
	global_load_lds_dwordx4 v[164:165], off
	s_add_i32 m0, s28, 0x2000
	s_add_u32 s26, s26, 0x40080
	v_lshl_add_u64 v[164:165], v[224:225], 0, s[10:11]
	s_addc_u32 s27, s27, 0
	s_add_i32 s28, s62, s2
	global_load_lds_dwordx4 v[164:165], off
	v_lshl_add_u64 v[164:165], s[26:27], 0, v[134:135]
	s_mov_b32 m0, s28
	s_nop 0
	global_load_lds_dwordx4 v[164:165], off
	v_lshl_add_u64 v[164:165], s[26:27], 0, v[130:131]
	s_add_i32 m0, s28, 0x2000
	s_nop 0
	global_load_lds_dwordx4 v[164:165], off
	v_lshl_add_u64 v[164:165], v[226:227], 0, s[10:11]
	s_mov_b32 m0, s37
	s_nop 0
	global_load_lds_dwordx4 v[164:165], off
	v_lshl_add_u64 v[164:165], v[230:231], 0, s[10:11]
	s_mov_b32 m0, s38
	s_nop 0
	global_load_lds_dwordx4 v[164:165], off
	s_waitcnt vmcnt(8)
	s_waitcnt lgkmcnt(0)
	s_barrier
	s_setprio 1
	s_waitcnt lgkmcnt(0)
	v_mfma_f32_16x16x32_bf16 v[62:65], v[148:151], v[192:195], v[62:65]
	v_mfma_f32_16x16x32_bf16 v[58:61], v[156:159], v[192:195], v[58:61]
	v_mfma_f32_16x16x32_bf16 v[50:53], v[148:151], v[200:203], v[50:53]
	v_mfma_f32_16x16x32_bf16 v[42:45], v[156:159], v[200:203], v[42:45]
	v_mfma_f32_16x16x32_bf16 v[34:37], v[148:151], v[208:211], v[34:37]
	v_mfma_f32_16x16x32_bf16 v[26:29], v[156:159], v[208:211], v[26:29]
	v_mfma_f32_16x16x32_bf16 v[18:21], v[148:151], v[216:219], v[18:21]
	v_mfma_f32_16x16x32_bf16 v[10:13], v[156:159], v[216:219], v[10:13]
	v_mfma_f32_16x16x32_bf16 v[62:65], v[152:155], v[196:199], v[62:65]
	v_mfma_f32_16x16x32_bf16 v[58:61], v[160:163], v[196:199], v[58:61]
	v_mfma_f32_16x16x32_bf16 v[50:53], v[152:155], v[204:207], v[50:53]
	v_mfma_f32_16x16x32_bf16 v[42:45], v[160:163], v[204:207], v[42:45]
	v_mfma_f32_16x16x32_bf16 v[34:37], v[152:155], v[212:215], v[34:37]
	v_mfma_f32_16x16x32_bf16 v[26:29], v[160:163], v[212:215], v[26:29]
	v_mfma_f32_16x16x32_bf16 v[18:21], v[152:155], v[220:223], v[18:21]
	v_mfma_f32_16x16x32_bf16 v[10:13], v[160:163], v[220:223], v[10:13]
	s_setprio 0
	s_setprio 1
	v_mfma_f32_16x16x32_bf16 v[54:57], v[176:179], v[192:195], v[54:57]
	v_mfma_f32_16x16x32_bf16 v[46:49], v[184:187], v[192:195], v[46:49]
	v_mfma_f32_16x16x32_bf16 v[38:41], v[176:179], v[200:203], v[38:41]
	v_mfma_f32_16x16x32_bf16 v[30:33], v[184:187], v[200:203], v[30:33]
	v_mfma_f32_16x16x32_bf16 v[22:25], v[176:179], v[208:211], v[22:25]
	v_mfma_f32_16x16x32_bf16 v[14:17], v[184:187], v[208:211], v[14:17]
	v_mfma_f32_16x16x32_bf16 v[6:9], v[176:179], v[216:219], v[6:9]
	v_mfma_f32_16x16x32_bf16 v[2:5], v[184:187], v[216:219], v[2:5]
	v_mfma_f32_16x16x32_bf16 v[54:57], v[180:183], v[196:199], v[54:57]
	v_mfma_f32_16x16x32_bf16 v[46:49], v[188:191], v[196:199], v[46:49]
	v_mfma_f32_16x16x32_bf16 v[38:41], v[180:183], v[204:207], v[38:41]
	v_mfma_f32_16x16x32_bf16 v[30:33], v[188:191], v[204:207], v[30:33]
	v_mfma_f32_16x16x32_bf16 v[22:25], v[180:183], v[212:215], v[22:25]
	v_mfma_f32_16x16x32_bf16 v[14:17], v[188:191], v[212:215], v[14:17]
	v_mfma_f32_16x16x32_bf16 v[6:9], v[180:183], v[220:223], v[6:9]
	v_mfma_f32_16x16x32_bf16 v[2:5], v[188:191], v[220:223], v[2:5]
	s_setprio 0
	s_barrier
	s_add_i32 s60, s60, 2
	s_add_u32 s24, s24, 0x100
	s_addc_u32 s25, s25, 0
	s_add_u32 s58, s58, 0x100
	s_addc_u32 s59, s59, 0
	s_cmp_gt_u32 s60, 13
	s_cbranch_scc0 .LBB0_253
	v_lshl_add_u32 v164, s22, 8, v167
	v_ashrrev_i32_e32 v165, 31, v164
	v_lshlrev_b64 v[148:149], 6, v[164:165]
	v_lshl_add_u64 v[148:149], v[138:139], 0, v[148:149]
	v_add_co_u32_e32 v150, vcc, 0x2000, v148
	v_addc_co_u32_e32 v151, vcc, 0, v149, vcc
	global_load_dwordx4 v[176:179], v[148:149], off
	global_load_dwordx4 v[180:183], v[148:149], off offset:1024
	global_load_dwordx4 v[184:187], v[148:149], off offset:2048
	global_load_dwordx4 v[188:191], v[148:149], off offset:3072
	global_load_dwordx4 v[192:195], v[150:151], off
	global_load_dwordx4 v[196:199], v[150:151], off offset:1024
	global_load_dwordx4 v[200:203], v[150:151], off offset:2048
	global_load_dwordx4 v[204:207], v[150:151], off offset:3072
	s_and_b64 vcc, exec, s[12:13]
	s_cbranch_vccz .LBB0_256
	s_barrier
; __device__ __forceinline__ unsigned cvt_pk_bf16(float lo, float hi) { const f32x2c_t v = {lo, hi}; return __builtin_bit_cast(unsigned, __builtin_convertvector(v, bf16x2c_t)); }
; __device__ __forceinline__ void rstd8(const float* SS, int rowb, int lane, float (&rs)[2][4]) {
;     f32x4 p[2][4];
; #pragma unroll
;     for (int ai = 0; ai < 2; ++ai)
; #pragma unroll
;         for (int m = 0; m < 4; ++m) p[ai][m] = *(const f32x4*)(SS + (size_t)(rowb + HALF * ai + 16 * m + (lane >> 2)) * 16 + 4 * (lane & 3));
;     asm volatile("" : "+v"(p[0][0]), "+v"(p[0][1]), "+v"(p[0][2]), "+v"(p[0][3]), "+v"(p[1][0]), "+v"(p[1][1]), "+v"(p[1][2]), "+v"(p[1][3]));
; #pragma unroll
;     for (int ai = 0; ai < 2; ++ai)
; #pragma unroll
;         for (int m = 0; m < 4; ++m) { float s = (p[ai][m][0] + p[ai][m][1]) + (p[ai][m][2] + p[ai][m][3]); s += __shfl_xor(s, 1); s += __shfl_xor(s, 2);
;             const float r = __builtin_amdgcn_rsqf(s * (1.0f / 1024.0f) + RMS_EPS);
;             rs[ai][m] = __builtin_bit_cast(float, __builtin_amdgcn_ds_bpermute((lane & 15) << 4, __builtin_bit_cast(int, r))); }
; }
;     __device__ __forceinline__ void operator()(const f32x4 (&acc)[2][2][4][2], const Unit& u, int wr, int wc, int fr, int fq) const {
;         const int row0 = u.pm * BM + wr * 64 + fr, col0 = u.pn * BM + wc * 32 + 8 * fq;
;         const float sc = (u.pn == 0) ? qs : ((u.pn == 3) ? 0.125f : 1.0f);
;         const int lane = fr + 16 * fq, qs4 = QSRC_ST(lane); const int rowS = u.pm * BM + wr * 64 + (lane >> 2), colS = u.pn * BM + wc * 32 + 8 * (lane & 3);
;         float rs8[2][4]; rstd8(SS, u.pm * BM + wr * 64, lane, rs8);
; #pragma unroll
;         for (int ai = 0; ai < 2; ++ai) {
; #pragma unroll
;             for (int m = 0; m < 4; ++m) { const float rs = rs8[ai][m] * sc;
;                 bf16_t* rowp = U + (size_t)(rowS + ai * HALF + m * 16) * ldu + colS;
; #pragma unroll
;                 for (int bj = 0; bj < 2; ++bj) { const f32x4 v0 = acc[ai][bj][m][0] * rs, v1 = acc[ai][bj][m][1] * rs;
;                     u32x4 w; w.x = cvt_pk_bf16(v0[0], v0[1]); w.y = cvt_pk_bf16(v0[2], v0[3]); w.z = cvt_pk_bf16(v1[0], v1[1]); w.w = cvt_pk_bf16(v1[2], v1[3]);
;                     *(u32x4*)(rowp + bj * HALF) = lane_perm(w, qs4); } } }
.LBB0_256:
	s_cmp_eq_u32 s49, 3
	s_cselect_b64 vcc, -1, 0
	v_cndmask_b32_e32 v156, 1.0, v174, vcc
	s_cmp_lg_u32 s49, 0
	s_cselect_b64 vcc, -1, 0
	v_cndmask_b32_e32 v156, v175, v156, vcc
	v_lshl_or_b32 v208, s49, 8, v169
	v_ashrrev_i32_e32 v209, 31, v208
	v_mov_b64_e32 v[154:155], s[44:45]
	v_lshlrev_b64 v[208:209], 1, v[208:209]
	v_mad_i64_i32 v[152:153], s[24:25], v164, s48, v[154:155]
	s_nop 0
	v_lshl_add_u64 v[208:209], v[152:153], 0, v[208:209]
	s_waitcnt vmcnt(0)
	v_add_f32_e32 v176, v176, v177
	v_add_f32_e32 v180, v180, v181
	v_add_f32_e32 v184, v184, v185
	v_add_f32_e32 v188, v188, v189
	v_add_f32_e32 v192, v192, v193
	v_add_f32_e32 v196, v196, v197
	v_add_f32_e32 v200, v200, v201
	v_add_f32_e32 v204, v204, v205
	v_add_f32_e32 v178, v178, v179
	v_add_f32_e32 v182, v182, v183
	v_add_f32_e32 v186, v186, v187
	v_add_f32_e32 v190, v190, v191
	v_add_f32_e32 v194, v194, v195
	v_add_f32_e32 v198, v198, v199
	v_add_f32_e32 v202, v202, v203
	v_add_f32_e32 v206, v206, v207
	v_add_f32_e32 v176, v176, v178
	v_add_f32_e32 v180, v180, v182
	v_add_f32_e32 v184, v184, v186
	v_add_f32_e32 v188, v188, v190
	v_add_f32_e32 v192, v192, v194
	v_add_f32_e32 v196, v196, v198
	v_add_f32_e32 v200, v200, v202
	v_add_f32_e32 v204, v204, v206
	v_add_f32_dpp v176, v176, v176 quad_perm:[1,0,3,2] row_mask:0xf bank_mask:0xf
	v_add_f32_dpp v180, v180, v180 quad_perm:[1,0,3,2] row_mask:0xf bank_mask:0xf
	v_add_f32_dpp v184, v184, v184 quad_perm:[1,0,3,2] row_mask:0xf bank_mask:0xf
	v_add_f32_dpp v188, v188, v188 quad_perm:[1,0,3,2] row_mask:0xf bank_mask:0xf
	v_add_f32_dpp v192, v192, v192 quad_perm:[1,0,3,2] row_mask:0xf bank_mask:0xf
	v_add_f32_dpp v196, v196, v196 quad_perm:[1,0,3,2] row_mask:0xf bank_mask:0xf
	v_add_f32_dpp v200, v200, v200 quad_perm:[1,0,3,2] row_mask:0xf bank_mask:0xf
	v_add_f32_dpp v204, v204, v204 quad_perm:[1,0,3,2] row_mask:0xf bank_mask:0xf
	v_add_f32_dpp v176, v176, v176 quad_perm:[2,3,0,1] row_mask:0xf bank_mask:0xf
	v_add_f32_dpp v180, v180, v180 quad_perm:[2,3,0,1] row_mask:0xf bank_mask:0xf
	v_add_f32_dpp v184, v184, v184 quad_perm:[2,3,0,1] row_mask:0xf bank_mask:0xf
	v_add_f32_dpp v188, v188, v188 quad_perm:[2,3,0,1] row_mask:0xf bank_mask:0xf
	v_add_f32_dpp v192, v192, v192 quad_perm:[2,3,0,1] row_mask:0xf bank_mask:0xf
	v_add_f32_dpp v196, v196, v196 quad_perm:[2,3,0,1] row_mask:0xf bank_mask:0xf
	v_add_f32_dpp v200, v200, v200 quad_perm:[2,3,0,1] row_mask:0xf bank_mask:0xf
	v_add_f32_dpp v204, v204, v204 quad_perm:[2,3,0,1] row_mask:0xf bank_mask:0xf
	v_fmamk_f32 v176, v176, 0x3a800000, v173
	v_fmamk_f32 v180, v180, 0x3a800000, v173
	v_fmamk_f32 v184, v184, 0x3a800000, v173
	v_fmamk_f32 v188, v188, 0x3a800000, v173
	v_fmamk_f32 v192, v192, 0x3a800000, v173
	v_fmamk_f32 v196, v196, 0x3a800000, v173
	v_fmamk_f32 v200, v200, 0x3a800000, v173
	v_fmamk_f32 v204, v204, 0x3a800000, v173
	ds_bpermute_b32 v176, v168, v176
	ds_bpermute_b32 v180, v168, v180
	ds_bpermute_b32 v184, v168, v184
	ds_bpermute_b32 v188, v168, v188
	ds_bpermute_b32 v192, v168, v192
	ds_bpermute_b32 v196, v168, v196
	ds_bpermute_b32 v200, v168, v200
	ds_bpermute_b32 v204, v168, v204
	s_waitcnt lgkmcnt(0)
	v_rsq_f32_e32 v178, v176
	v_rsq_f32_e32 v182, v180
	v_rsq_f32_e32 v186, v184
	v_rsq_f32_e32 v190, v188
	v_rsq_f32_e32 v194, v192
	v_rsq_f32_e32 v198, v196
	v_rsq_f32_e32 v202, v200
	v_rsq_f32_e32 v206, v204
	v_mul_f32_e32 v178, v156, v178
	v_mul_f32_e32 v182, v156, v182
	v_mul_f32_e32 v186, v156, v186
	v_mul_f32_e32 v190, v156, v190
	v_mul_f32_e32 v194, v156, v194
	v_mul_f32_e32 v198, v156, v198
	v_mul_f32_e32 v202, v156, v202
	v_mul_f32_e32 v206, v156, v206
	v_pk_mul_f32 v[126:127], v[126:127], v[178:179] op_sel_hi:[1,0]
	v_pk_mul_f32 v[128:129], v[128:129], v[178:179] op_sel_hi:[1,0]
	v_pk_mul_f32 v[122:123], v[122:123], v[178:179] op_sel_hi:[1,0]
	v_pk_mul_f32 v[124:125], v[124:125], v[178:179] op_sel_hi:[1,0]
	v_pk_mul_f32 v[118:119], v[118:119], v[178:179] op_sel_hi:[1,0]
	v_pk_mul_f32 v[120:121], v[120:121], v[178:179] op_sel_hi:[1,0]
	v_pk_mul_f32 v[110:111], v[110:111], v[178:179] op_sel_hi:[1,0]
	v_pk_mul_f32 v[112:113], v[112:113], v[178:179] op_sel_hi:[1,0]
	v_cvt_pk_bf16_f32 v126, v126, v127
	v_cvt_pk_bf16_f32 v127, v128, v129
	v_cvt_pk_bf16_f32 v128, v122, v123
	v_cvt_pk_bf16_f32 v129, v124, v125
	v_cvt_pk_bf16_f32 v118, v118, v119
	v_cvt_pk_bf16_f32 v119, v120, v121
	v_cvt_pk_bf16_f32 v120, v110, v111
	v_cvt_pk_bf16_f32 v121, v112, v113
	ds_bpermute_b32 v122, v166, v126
	ds_bpermute_b32 v123, v166, v127
	ds_bpermute_b32 v124, v166, v128
	ds_bpermute_b32 v125, v166, v129
	ds_bpermute_b32 v110, v166, v118
	ds_bpermute_b32 v111, v166, v119
	ds_bpermute_b32 v112, v166, v120
	ds_bpermute_b32 v113, v166, v121
	v_mov_b32_e32 v210, v208
	v_mov_b32_e32 v211, v209
	v_pk_mul_f32 v[114:115], v[114:115], v[182:183] op_sel_hi:[1,0]
	v_pk_mul_f32 v[116:117], v[116:117], v[182:183] op_sel_hi:[1,0]
	v_pk_mul_f32 v[106:107], v[106:107], v[182:183] op_sel_hi:[1,0]
	v_pk_mul_f32 v[108:109], v[108:109], v[182:183] op_sel_hi:[1,0]
	v_pk_mul_f32 v[102:103], v[102:103], v[182:183] op_sel_hi:[1,0]
	v_pk_mul_f32 v[104:105], v[104:105], v[182:183] op_sel_hi:[1,0]
	v_pk_mul_f32 v[94:95], v[94:95], v[182:183] op_sel_hi:[1,0]
	v_pk_mul_f32 v[96:97], v[96:97], v[182:183] op_sel_hi:[1,0]
	v_cvt_pk_bf16_f32 v114, v114, v115
	v_cvt_pk_bf16_f32 v115, v116, v117
	v_cvt_pk_bf16_f32 v116, v106, v107
	v_cvt_pk_bf16_f32 v117, v108, v109
	v_cvt_pk_bf16_f32 v102, v102, v103
	v_cvt_pk_bf16_f32 v103, v104, v105
	v_cvt_pk_bf16_f32 v104, v94, v95
	v_cvt_pk_bf16_f32 v105, v96, v97
	ds_bpermute_b32 v106, v166, v114
	ds_bpermute_b32 v107, v166, v115
	ds_bpermute_b32 v108, v166, v116
	ds_bpermute_b32 v109, v166, v117
	ds_bpermute_b32 v94, v166, v102
	ds_bpermute_b32 v95, v166, v103
	ds_bpermute_b32 v96, v166, v104
	ds_bpermute_b32 v97, v166, v105
	v_add_co_u32_e32 v212, vcc, 0x18000, v208
	v_addc_co_u32_e32 v213, vcc, 0, v209, vcc
	s_waitcnt lgkmcnt(8)
; __device__ __forceinline__ unsigned cvt_pk_bf16(float lo, float hi) { const f32x2c_t v = {lo, hi}; return __builtin_bit_cast(unsigned, __builtin_convertvector(v, bf16x2c_t)); }
;     __device__ __forceinline__ void operator()(const f32x4 (&acc)[2][2][4][2], const Unit& u, int wr, int wc, int fr, int fq) const {
;     ...
;         for (int ai = 0; ai < 2; ++ai) {
; #pragma unroll
;             for (int m = 0; m < 4; ++m) { const float rs = rs8[ai][m] * sc;
;                 bf16_t* rowp = U + (size_t)(rowS + ai * HALF + m * 16) * ldu + colS;
; #pragma unroll
;                 for (int bj = 0; bj < 2; ++bj) { const f32x4 v0 = acc[ai][bj][m][0] * rs, v1 = acc[ai][bj][m][1] * rs;
;                     u32x4 w; w.x = cvt_pk_bf16(v0[0], v0[1]); w.y = cvt_pk_bf16(v0[2], v0[3]); w.z = cvt_pk_bf16(v1[0], v1[1]); w.w = cvt_pk_bf16(v1[2], v1[3]);
;                     *(u32x4*)(rowp + bj * HALF) = lane_perm(w, qs4); } } }
	global_store_dwordx4 v[210:211], v[122:125], off
	global_store_dwordx4 v[210:211], v[110:113], off offset:256
	v_pk_mul_f32 v[98:99], v[98:99], v[186:187] op_sel_hi:[1,0]
	v_pk_mul_f32 v[100:101], v[100:101], v[186:187] op_sel_hi:[1,0]
	v_pk_mul_f32 v[90:91], v[90:91], v[186:187] op_sel_hi:[1,0]
	v_pk_mul_f32 v[92:93], v[92:93], v[186:187] op_sel_hi:[1,0]
	v_pk_mul_f32 v[86:87], v[86:87], v[186:187] op_sel_hi:[1,0]
	v_pk_mul_f32 v[88:89], v[88:89], v[186:187] op_sel_hi:[1,0]
	v_pk_mul_f32 v[78:79], v[78:79], v[186:187] op_sel_hi:[1,0]
	v_pk_mul_f32 v[80:81], v[80:81], v[186:187] op_sel_hi:[1,0]
	v_cvt_pk_bf16_f32 v98, v98, v99
	v_cvt_pk_bf16_f32 v99, v100, v101
	v_cvt_pk_bf16_f32 v100, v90, v91
	v_cvt_pk_bf16_f32 v101, v92, v93
	v_cvt_pk_bf16_f32 v86, v86, v87
	v_cvt_pk_bf16_f32 v87, v88, v89
	v_cvt_pk_bf16_f32 v88, v78, v79
	v_cvt_pk_bf16_f32 v89, v80, v81
	ds_bpermute_b32 v90, v166, v98
	ds_bpermute_b32 v91, v166, v99
	ds_bpermute_b32 v92, v166, v100
	ds_bpermute_b32 v93, v166, v101
	ds_bpermute_b32 v78, v166, v86
	ds_bpermute_b32 v79, v166, v87
	ds_bpermute_b32 v80, v166, v88
	ds_bpermute_b32 v81, v166, v89
	v_add_co_u32_e32 v210, vcc, 0x30000, v208
	v_addc_co_u32_e32 v211, vcc, 0, v209, vcc
	s_waitcnt lgkmcnt(8)
	global_store_dwordx4 v[212:213], v[106:109], off
	global_store_dwordx4 v[212:213], v[94:97], off offset:256
	v_pk_mul_f32 v[82:83], v[82:83], v[190:191] op_sel_hi:[1,0]
	v_pk_mul_f32 v[84:85], v[84:85], v[190:191] op_sel_hi:[1,0]
	v_pk_mul_f32 v[74:75], v[74:75], v[190:191] op_sel_hi:[1,0]
	v_pk_mul_f32 v[76:77], v[76:77], v[190:191] op_sel_hi:[1,0]
	v_pk_mul_f32 v[70:71], v[70:71], v[190:191] op_sel_hi:[1,0]
	v_pk_mul_f32 v[72:73], v[72:73], v[190:191] op_sel_hi:[1,0]
	v_pk_mul_f32 v[66:67], v[66:67], v[190:191] op_sel_hi:[1,0]
	v_pk_mul_f32 v[68:69], v[68:69], v[190:191] op_sel_hi:[1,0]
	v_cvt_pk_bf16_f32 v82, v82, v83
	v_cvt_pk_bf16_f32 v83, v84, v85
	v_cvt_pk_bf16_f32 v84, v74, v75
	v_cvt_pk_bf16_f32 v85, v76, v77
	v_cvt_pk_bf16_f32 v70, v70, v71
	v_cvt_pk_bf16_f32 v71, v72, v73
	v_cvt_pk_bf16_f32 v72, v66, v67
	v_cvt_pk_bf16_f32 v73, v68, v69
	ds_bpermute_b32 v74, v166, v82
	ds_bpermute_b32 v75, v166, v83
	ds_bpermute_b32 v76, v166, v84
	ds_bpermute_b32 v77, v166, v85
	ds_bpermute_b32 v66, v166, v70
	ds_bpermute_b32 v67, v166, v71
	ds_bpermute_b32 v68, v166, v72
	ds_bpermute_b32 v69, v166, v73
	v_add_co_u32_e32 v212, vcc, 0x48000, v208
	v_addc_co_u32_e32 v213, vcc, 0, v209, vcc
	s_waitcnt lgkmcnt(8)
	global_store_dwordx4 v[210:211], v[90:93], off
	global_store_dwordx4 v[210:211], v[78:81], off offset:256
	v_pk_mul_f32 v[62:63], v[62:63], v[194:195] op_sel_hi:[1,0]
	v_pk_mul_f32 v[64:65], v[64:65], v[194:195] op_sel_hi:[1,0]
	v_pk_mul_f32 v[58:59], v[58:59], v[194:195] op_sel_hi:[1,0]
	v_pk_mul_f32 v[60:61], v[60:61], v[194:195] op_sel_hi:[1,0]
	v_pk_mul_f32 v[54:55], v[54:55], v[194:195] op_sel_hi:[1,0]
	v_pk_mul_f32 v[56:57], v[56:57], v[194:195] op_sel_hi:[1,0]
	v_pk_mul_f32 v[46:47], v[46:47], v[194:195] op_sel_hi:[1,0]
	v_pk_mul_f32 v[48:49], v[48:49], v[194:195] op_sel_hi:[1,0]
	v_cvt_pk_bf16_f32 v62, v62, v63
	v_cvt_pk_bf16_f32 v63, v64, v65
	v_cvt_pk_bf16_f32 v64, v58, v59
	v_cvt_pk_bf16_f32 v65, v60, v61
	v_cvt_pk_bf16_f32 v54, v54, v55
	v_cvt_pk_bf16_f32 v55, v56, v57
	v_cvt_pk_bf16_f32 v56, v46, v47
	v_cvt_pk_bf16_f32 v57, v48, v49
	ds_bpermute_b32 v58, v166, v62
	ds_bpermute_b32 v59, v166, v63
	ds_bpermute_b32 v60, v166, v64
	ds_bpermute_b32 v61, v166, v65
	ds_bpermute_b32 v46, v166, v54
	ds_bpermute_b32 v47, v166, v55
	ds_bpermute_b32 v48, v166, v56
	ds_bpermute_b32 v49, v166, v57
	v_add_co_u32_e32 v210, vcc, 0xc0000, v208
	v_addc_co_u32_e32 v211, vcc, 0, v209, vcc
	s_waitcnt lgkmcnt(8)
; __device__ __forceinline__ unsigned cvt_pk_bf16(float lo, float hi) { const f32x2c_t v = {lo, hi}; return __builtin_bit_cast(unsigned, __builtin_convertvector(v, bf16x2c_t)); }
;     __device__ __forceinline__ void operator()(const f32x4 (&acc)[2][2][4][2], const Unit& u, int wr, int wc, int fr, int fq) const {
;     ...
;         for (int ai = 0; ai < 2; ++ai) {
; #pragma unroll
;             for (int m = 0; m < 4; ++m) { const float rs = rs8[ai][m] * sc;
;                 bf16_t* rowp = U + (size_t)(rowS + ai * HALF + m * 16) * ldu + colS;
; #pragma unroll
;                 for (int bj = 0; bj < 2; ++bj) { const f32x4 v0 = acc[ai][bj][m][0] * rs, v1 = acc[ai][bj][m][1] * rs;
;                     u32x4 w; w.x = cvt_pk_bf16(v0[0], v0[1]); w.y = cvt_pk_bf16(v0[2], v0[3]); w.z = cvt_pk_bf16(v1[0], v1[1]); w.w = cvt_pk_bf16(v1[2], v1[3]);
;                     *(u32x4*)(rowp + bj * HALF) = lane_perm(w, qs4); } } }
; template <class Epi, class Sched, bool ALIGN_EPI = false, bool SP2 = false>
; __device__ __forceinline__ void gemm_phase(PG8_LAS unsigned char* lds, const Gemm g, const Sched& S, const Epi& E, const bool skip_epi = false) {
;     ...
;         if (!has_next) break;
	global_store_dwordx4 v[212:213], v[74:77], off
	global_store_dwordx4 v[212:213], v[66:69], off offset:256
	v_pk_mul_f32 v[50:51], v[50:51], v[198:199] op_sel_hi:[1,0]
	v_pk_mul_f32 v[52:53], v[52:53], v[198:199] op_sel_hi:[1,0]
	v_pk_mul_f32 v[42:43], v[42:43], v[198:199] op_sel_hi:[1,0]
	v_pk_mul_f32 v[44:45], v[44:45], v[198:199] op_sel_hi:[1,0]
	v_pk_mul_f32 v[38:39], v[38:39], v[198:199] op_sel_hi:[1,0]
	v_pk_mul_f32 v[40:41], v[40:41], v[198:199] op_sel_hi:[1,0]
	v_pk_mul_f32 v[30:31], v[30:31], v[198:199] op_sel_hi:[1,0]
	v_pk_mul_f32 v[32:33], v[32:33], v[198:199] op_sel_hi:[1,0]
	v_cvt_pk_bf16_f32 v50, v50, v51
	v_cvt_pk_bf16_f32 v51, v52, v53
	v_cvt_pk_bf16_f32 v52, v42, v43
	v_cvt_pk_bf16_f32 v53, v44, v45
	v_cvt_pk_bf16_f32 v38, v38, v39
	v_cvt_pk_bf16_f32 v39, v40, v41
	v_cvt_pk_bf16_f32 v40, v30, v31
	v_cvt_pk_bf16_f32 v41, v32, v33
	ds_bpermute_b32 v42, v166, v50
	ds_bpermute_b32 v43, v166, v51
	ds_bpermute_b32 v44, v166, v52
	ds_bpermute_b32 v45, v166, v53
	ds_bpermute_b32 v30, v166, v38
	ds_bpermute_b32 v31, v166, v39
	ds_bpermute_b32 v32, v166, v40
	ds_bpermute_b32 v33, v166, v41
	v_add_co_u32_e32 v212, vcc, 0xd8000, v208
	v_addc_co_u32_e32 v213, vcc, 0, v209, vcc
	s_waitcnt lgkmcnt(8)
	global_store_dwordx4 v[210:211], v[58:61], off
	global_store_dwordx4 v[210:211], v[46:49], off offset:256
	v_pk_mul_f32 v[34:35], v[34:35], v[202:203] op_sel_hi:[1,0]
	v_pk_mul_f32 v[36:37], v[36:37], v[202:203] op_sel_hi:[1,0]
	v_pk_mul_f32 v[26:27], v[26:27], v[202:203] op_sel_hi:[1,0]
	v_pk_mul_f32 v[28:29], v[28:29], v[202:203] op_sel_hi:[1,0]
	v_pk_mul_f32 v[22:23], v[22:23], v[202:203] op_sel_hi:[1,0]
	v_pk_mul_f32 v[24:25], v[24:25], v[202:203] op_sel_hi:[1,0]
	v_pk_mul_f32 v[14:15], v[14:15], v[202:203] op_sel_hi:[1,0]
	v_pk_mul_f32 v[16:17], v[16:17], v[202:203] op_sel_hi:[1,0]
	v_cvt_pk_bf16_f32 v34, v34, v35
	v_cvt_pk_bf16_f32 v35, v36, v37
	v_cvt_pk_bf16_f32 v36, v26, v27
	v_cvt_pk_bf16_f32 v37, v28, v29
	v_cvt_pk_bf16_f32 v22, v22, v23
	v_cvt_pk_bf16_f32 v23, v24, v25
	v_cvt_pk_bf16_f32 v24, v14, v15
	v_cvt_pk_bf16_f32 v25, v16, v17
	ds_bpermute_b32 v26, v166, v34
	ds_bpermute_b32 v27, v166, v35
	ds_bpermute_b32 v28, v166, v36
	ds_bpermute_b32 v29, v166, v37
	ds_bpermute_b32 v14, v166, v22
	ds_bpermute_b32 v15, v166, v23
	ds_bpermute_b32 v16, v166, v24
	ds_bpermute_b32 v17, v166, v25
	v_add_co_u32_e32 v210, vcc, 0xf0000, v208
	v_addc_co_u32_e32 v211, vcc, 0, v209, vcc
	s_waitcnt lgkmcnt(8)
	global_store_dwordx4 v[212:213], v[42:45], off
	global_store_dwordx4 v[212:213], v[30:33], off offset:256
	v_pk_mul_f32 v[18:19], v[18:19], v[206:207] op_sel_hi:[1,0]
	v_pk_mul_f32 v[20:21], v[20:21], v[206:207] op_sel_hi:[1,0]
	v_pk_mul_f32 v[10:11], v[10:11], v[206:207] op_sel_hi:[1,0]
	v_pk_mul_f32 v[12:13], v[12:13], v[206:207] op_sel_hi:[1,0]
	v_pk_mul_f32 v[6:7], v[6:7], v[206:207] op_sel_hi:[1,0]
	v_pk_mul_f32 v[8:9], v[8:9], v[206:207] op_sel_hi:[1,0]
	v_pk_mul_f32 v[2:3], v[2:3], v[206:207] op_sel_hi:[1,0]
	v_pk_mul_f32 v[4:5], v[4:5], v[206:207] op_sel_hi:[1,0]
	v_cvt_pk_bf16_f32 v18, v18, v19
	v_cvt_pk_bf16_f32 v19, v20, v21
	v_cvt_pk_bf16_f32 v20, v10, v11
	v_cvt_pk_bf16_f32 v21, v12, v13
	v_cvt_pk_bf16_f32 v6, v6, v7
	v_cvt_pk_bf16_f32 v7, v8, v9
	v_cvt_pk_bf16_f32 v8, v2, v3
	v_cvt_pk_bf16_f32 v9, v4, v5
	ds_bpermute_b32 v10, v166, v18
	ds_bpermute_b32 v11, v166, v19
	ds_bpermute_b32 v12, v166, v20
	ds_bpermute_b32 v13, v166, v21
	ds_bpermute_b32 v2, v166, v6
	ds_bpermute_b32 v3, v166, v7
	ds_bpermute_b32 v4, v166, v8
	ds_bpermute_b32 v5, v166, v9
	v_add_co_u32_e32 v212, vcc, 0x108000, v208
	v_addc_co_u32_e32 v213, vcc, 0, v209, vcc
	s_waitcnt lgkmcnt(8)
	global_store_dwordx4 v[210:211], v[26:29], off
	global_store_dwordx4 v[210:211], v[14:17], off offset:256
	s_waitcnt lgkmcnt(0)
	global_store_dwordx4 v[212:213], v[10:13], off
	global_store_dwordx4 v[212:213], v[2:5], off offset:256
	s_andn2_b64 vcc, exec, s[4:5]
	s_mov_b64 s[4:5], -1
	s_cbranch_vccnz .LBB0_249
	s_andn2_b64 vcc, exec, s[6:7]
	s_cbranch_vccnz .LBB0_248
	s_barrier
	s_branch .LBB0_248

; #define PG8_STAGE_A(b, h, ptr, NX) do { if constexpr (Sched::GATHER) { unsigned gs_[2]; gs_[0] = ((NX) && last_) ? gN[h][0] : gA[h][0]; gs_[1] = ((NX) && last_) ? gN[h][1] : gA[h][1]; PG8_STAGE(PG8_SA(b, h), ptr, gs_); } \
;         else PG8_STAGE(PG8_SA(b, h), (ptr) + ((h) ? hstep : (size_t)0), voffA); } while (0)
; #define PG8_STAGE(bufoff, gbase, voff) do { _Pragma("unroll") for (int _i = 0; _i < 2; ++_i) \
;         __builtin_amdgcn_global_load_lds((const unsigned*)((const char*)(gbase) + (voff)[_i]), (PG8_LAS unsigned*)(lds + (bufoff) + ldsw + _i * 8192), 16, 0, 0); } while (0)
; #define PG8_WAIT_V(n) asm volatile("s_waitcnt vmcnt(" #n ")" ::: "memory")
; #define PG8_BAR __builtin_amdgcn_s_barrier()
; template <class Epi, class Sched, bool ALIGN_EPI = false, bool SP2 = false>
; __device__ __forceinline__ void gemm_phase(PG8_LAS unsigned char* lds, const Gemm g, const Sched& S, const Epi& E, const bool skip_epi = false) {
;     ...
;         for (int t = 0; t < nt; t += 2) {
;             const bool last = (t == nt - 2); last_ = last && has_next;
;             const char* a1 = cA + (size_t)(t + 1) * kstep;
;             const char* a2 = last ? nA : cA + (size_t)(t + 2) * kstep; const char* b2 = last ? nB : cB + (size_t)(t + 2) * kstep;
;             const char* a3 = a2 + kstep; const char* b3 = b2 + kstep;
;             if (last && has_next) S.a_ready(nxt);
;             if constexpr (SP2) {
;             PG8_LDB(B0, 0, 0); PG8_LDB(B1, 0, 1); PG8_SCHED; PG8_LDA(At, 0, 0); PG8_STAGE_A(1, 1, a1, false);
;             PG8_WAIT_V(8); PG8_WAIT_L(0); PG8_BAR; PG8_MMA(0, 0, At, B0); PG8_MMA(0, 1, At, B1); PG8_BAR; PG8_SCHED;
;             PG8_LDA(At, 0, 1); PG8_STAGE(PG8_SB(0, 0), b2, voffB); PG8_STAGE(PG8_SB(0, 1), b2 + hstep, voffB); PG8_STAGE_A(0, 0, a2, true);
;             PG8_WAIT_V(8); PG8_WAIT_L(0); PG8_BAR; PG8_MMA(1, 0, At, B0); PG8_MMA(1, 1, At, B1); PG8_BAR; PG8_SCHED;
;             PG8_LDB(B0, 1, 0); PG8_LDB(B1, 1, 1); PG8_SCHED; PG8_LDA(At, 1, 0); PG8_STAGE_A(0, 1, a2, true);
;             PG8_WAIT_V(8); PG8_WAIT_L(0); PG8_BAR; PG8_MMA(0, 0, At, B0); PG8_MMA(0, 1, At, B1); PG8_BAR; PG8_SCHED;
;             PG8_LDA(At, 1, 1); PG8_STAGE(PG8_SB(1, 0), b3, voffB); PG8_STAGE(PG8_SB(1, 1), b3 + hstep, voffB); PG8_STAGE_A(1, 0, a3, true);
;             PG8_WAIT_V(8); PG8_WAIT_L(0); PG8_BAR; PG8_MMA(1, 0, At, B0); PG8_MMA(1, 1, At, B1); PG8_BAR; PG8_SCHED;
.LBB0_944:
	ds_read_b128 v[148:151], v170
	ds_read_b128 v[152:155], v170 offset:1024
	ds_read_b128 v[156:159], v170 offset:2048
	ds_read_b128 v[160:163], v170 offset:3072
	ds_read_b128 v[176:179], v171
	ds_read_b128 v[180:183], v171 offset:1024
	ds_read_b128 v[184:187], v171 offset:2048
	ds_read_b128 v[188:191], v171 offset:3072
	s_add_u32 s24, s22, 0xfffc0080
	s_addc_u32 s25, s23, -1
	s_cmp_eq_u32 s58, 12
	s_cselect_b32 s27, s15, s25
	s_cselect_b32 s26, s54, s24
	s_cselect_b32 s25, s13, s57
	s_cselect_b32 s24, s55, s56
	v_lshl_add_u64 v[164:165], s[22:23], 0, v[140:141]
	s_add_i32 m0, s21, 0xc000
	ds_read_b128 v[192:195], v172
	ds_read_b128 v[196:199], v172 offset:1024
	ds_read_b128 v[200:203], v172 offset:2048
	ds_read_b128 v[204:207], v172 offset:3072
	ds_read_b128 v[208:211], v172 offset:4096
	ds_read_b128 v[212:215], v172 offset:5120
	ds_read_b128 v[216:219], v172 offset:6144
	ds_read_b128 v[220:223], v172 offset:7168
	global_load_lds_dwordx4 v[164:165], off
	v_lshl_add_u64 v[164:165], s[22:23], 0, v[142:143]
	s_add_i32 m0, s21, 0xe000
	s_nop 0
	global_load_lds_dwordx4 v[164:165], off
	s_waitcnt vmcnt(8)
	s_waitcnt lgkmcnt(0)
	s_barrier
	s_setprio 1
	s_waitcnt lgkmcnt(0)
	v_mfma_f32_16x16x32_bf16 v[126:129], v[148:151], v[192:195], v[126:129]
	v_mfma_f32_16x16x32_bf16 v[122:125], v[156:159], v[192:195], v[122:125]
	v_mfma_f32_16x16x32_bf16 v[114:117], v[148:151], v[200:203], v[114:117]
	v_mfma_f32_16x16x32_bf16 v[106:109], v[156:159], v[200:203], v[106:109]
	v_mfma_f32_16x16x32_bf16 v[98:101], v[148:151], v[208:211], v[98:101]
	v_mfma_f32_16x16x32_bf16 v[90:93], v[156:159], v[208:211], v[90:93]
	v_mfma_f32_16x16x32_bf16 v[82:85], v[148:151], v[216:219], v[82:85]
	v_mfma_f32_16x16x32_bf16 v[74:77], v[156:159], v[216:219], v[74:77]
	v_mfma_f32_16x16x32_bf16 v[126:129], v[152:155], v[196:199], v[126:129]
	v_mfma_f32_16x16x32_bf16 v[122:125], v[160:163], v[196:199], v[122:125]
	v_mfma_f32_16x16x32_bf16 v[114:117], v[152:155], v[204:207], v[114:117]
	v_mfma_f32_16x16x32_bf16 v[106:109], v[160:163], v[204:207], v[106:109]
	v_mfma_f32_16x16x32_bf16 v[98:101], v[152:155], v[212:215], v[98:101]
	v_mfma_f32_16x16x32_bf16 v[90:93], v[160:163], v[212:215], v[90:93]
	v_mfma_f32_16x16x32_bf16 v[82:85], v[152:155], v[220:223], v[82:85]
	v_mfma_f32_16x16x32_bf16 v[74:77], v[160:163], v[220:223], v[74:77]
	s_setprio 0
	s_setprio 1
	v_mfma_f32_16x16x32_bf16 v[118:121], v[176:179], v[192:195], v[118:121]
	v_mfma_f32_16x16x32_bf16 v[110:113], v[184:187], v[192:195], v[110:113]
	v_mfma_f32_16x16x32_bf16 v[102:105], v[176:179], v[200:203], v[102:105]
	v_mfma_f32_16x16x32_bf16 v[94:97], v[184:187], v[200:203], v[94:97]
	v_mfma_f32_16x16x32_bf16 v[86:89], v[176:179], v[208:211], v[86:89]
	v_mfma_f32_16x16x32_bf16 v[78:81], v[184:187], v[208:211], v[78:81]
	v_mfma_f32_16x16x32_bf16 v[70:73], v[176:179], v[216:219], v[70:73]
	v_mfma_f32_16x16x32_bf16 v[66:69], v[184:187], v[216:219], v[66:69]
	v_mfma_f32_16x16x32_bf16 v[118:121], v[180:183], v[196:199], v[118:121]
	v_mfma_f32_16x16x32_bf16 v[110:113], v[188:191], v[196:199], v[110:113]
	v_mfma_f32_16x16x32_bf16 v[102:105], v[180:183], v[204:207], v[102:105]
	v_mfma_f32_16x16x32_bf16 v[94:97], v[188:191], v[204:207], v[94:97]
	v_mfma_f32_16x16x32_bf16 v[86:89], v[180:183], v[212:215], v[86:89]
	v_mfma_f32_16x16x32_bf16 v[78:81], v[188:191], v[212:215], v[78:81]
	v_mfma_f32_16x16x32_bf16 v[70:73], v[180:183], v[220:223], v[70:73]
	v_mfma_f32_16x16x32_bf16 v[66:69], v[188:191], v[220:223], v[66:69]
	s_setprio 0
	s_barrier
	s_add_i32 s59, s48, s28
	v_lshl_add_u64 v[164:165], s[24:25], 0, v[134:135]
	s_mov_b32 m0, s59
	ds_read_b128 v[192:195], v172 offset:16384
	ds_read_b128 v[196:199], v172 offset:17408
	ds_read_b128 v[200:203], v172 offset:18432
	ds_read_b128 v[204:207], v172 offset:19456
	ds_read_b128 v[208:211], v172 offset:20480
	ds_read_b128 v[212:215], v172 offset:21504
	ds_read_b128 v[216:219], v172 offset:22528
	ds_read_b128 v[220:223], v172 offset:23552
	global_load_lds_dwordx4 v[164:165], off
	s_add_i32 m0, s59, 0x2000
	s_add_u32 s60, s24, 0x40000
	v_lshl_add_u64 v[224:225], s[24:25], 0, v[130:131]
	s_addc_u32 s61, s25, 0
	s_add_i32 s59, s49, s28
	global_load_lds_dwordx4 v[224:225], off
	v_lshl_add_u64 v[226:227], s[60:61], 0, v[134:135]
	s_mov_b32 m0, s59
	v_lshl_add_u64 v[230:231], s[26:27], 0, v[132:133]
	global_load_lds_dwordx4 v[226:227], off
	v_lshl_add_u64 v[226:227], s[60:61], 0, v[130:131]
	s_add_i32 m0, s59, 0x2000
	s_nop 0
	global_load_lds_dwordx4 v[226:227], off
	v_lshl_add_u64 v[226:227], s[26:27], 0, v[136:137]
	s_mov_b32 m0, s21
	s_nop 0
	global_load_lds_dwordx4 v[226:227], off
	s_mov_b32 m0, s31
	s_nop 0
	global_load_lds_dwordx4 v[230:231], off
	s_waitcnt vmcnt(8)
	s_waitcnt lgkmcnt(0)
	s_barrier
; #define PG8_STAGE_A(b, h, ptr, NX) do { if constexpr (Sched::GATHER) { unsigned gs_[2]; gs_[0] = ((NX) && last_) ? gN[h][0] : gA[h][0]; gs_[1] = ((NX) && last_) ? gN[h][1] : gA[h][1]; PG8_STAGE(PG8_SA(b, h), ptr, gs_); } \
;         else PG8_STAGE(PG8_SA(b, h), (ptr) + ((h) ? hstep : (size_t)0), voffA); } while (0)
; #define PG8_STAGE(bufoff, gbase, voff) do { _Pragma("unroll") for (int _i = 0; _i < 2; ++_i) \
;         __builtin_amdgcn_global_load_lds((const unsigned*)((const char*)(gbase) + (voff)[_i]), (PG8_LAS unsigned*)(lds + (bufoff) + ldsw + _i * 8192), 16, 0, 0); } while (0)
; #define PG8_LDA(dst, b, h) do { _Pragma("unroll") for (int m = 0; m < 4; ++m) _Pragma("unroll") for (int k = 0; k < 2; ++k) dst[m][k] = *(const PG8_LAS bf16x8*)(lds + PG8_SA(b, h) + aoff + m * 2048 + k * 1024); } while (0)
; #define PG8_LDB(dst, b, h) do { _Pragma("unroll") for (int n = 0; n < 2; ++n) _Pragma("unroll") for (int k = 0; k < 2; ++k) dst[n][k] = *(const PG8_LAS bf16x8*)(lds + PG8_SB(b, h) + boff + n * 2048 + k * 1024); } while (0)
; #define PG8_MMA(ai, bj, At, Bt) do { __builtin_amdgcn_s_setprio(1); _Pragma("unroll") for (int m = 0; m < 4; ++m) _Pragma("unroll") for (int n = 0; n < 2; ++n) _Pragma("unroll") for (int k = 0; k < 2; ++k) \
;         acc[ai][bj][m][n] = __builtin_amdgcn_mfma_f32_16x16x32_bf16(Bt[n][k], At[m][k], acc[ai][bj][m][n], 0, 0, 0); __builtin_amdgcn_s_setprio(0); } while (0)
; template <class Epi, class Sched, bool ALIGN_EPI = false, bool SP2 = false>
; __device__ __forceinline__ void gemm_phase(PG8_LAS unsigned char* lds, const Gemm g, const Sched& S, const Epi& E, const bool skip_epi = false) {
;     ...
;             PG8_WAIT_V(8); PG8_WAIT_L(0); PG8_BAR; PG8_MMA(0, 0, At, B0); PG8_MMA(0, 1, At, B1); PG8_BAR; PG8_SCHED;
;             PG8_LDA(At, 0, 1); PG8_STAGE(PG8_SB(0, 0), b2, voffB); PG8_STAGE(PG8_SB(0, 1), b2 + hstep, voffB); PG8_STAGE_A(0, 0, a2, true);
;             PG8_WAIT_V(8); PG8_WAIT_L(0); PG8_BAR; PG8_MMA(1, 0, At, B0); PG8_MMA(1, 1, At, B1); PG8_BAR; PG8_SCHED;
;             PG8_LDB(B0, 1, 0); PG8_LDB(B1, 1, 1); PG8_SCHED; PG8_LDA(At, 1, 0); PG8_STAGE_A(0, 1, a2, true);
;             PG8_WAIT_V(8); PG8_WAIT_L(0); PG8_BAR; PG8_MMA(0, 0, At, B0); PG8_MMA(0, 1, At, B1); PG8_BAR; PG8_SCHED;
;             PG8_LDA(At, 1, 1); PG8_STAGE(PG8_SB(1, 0), b3, voffB); PG8_STAGE(PG8_SB(1, 1), b3 + hstep, voffB); PG8_STAGE_A(1, 0, a3, true);
	s_setprio 1
	s_waitcnt lgkmcnt(0)
	v_mfma_f32_16x16x32_bf16 v[62:65], v[148:151], v[192:195], v[62:65]
	v_mfma_f32_16x16x32_bf16 v[58:61], v[156:159], v[192:195], v[58:61]
	v_mfma_f32_16x16x32_bf16 v[50:53], v[148:151], v[200:203], v[50:53]
	v_mfma_f32_16x16x32_bf16 v[42:45], v[156:159], v[200:203], v[42:45]
	v_mfma_f32_16x16x32_bf16 v[34:37], v[148:151], v[208:211], v[34:37]
	v_mfma_f32_16x16x32_bf16 v[26:29], v[156:159], v[208:211], v[26:29]
	v_mfma_f32_16x16x32_bf16 v[18:21], v[148:151], v[216:219], v[18:21]
	v_mfma_f32_16x16x32_bf16 v[10:13], v[156:159], v[216:219], v[10:13]
	v_mfma_f32_16x16x32_bf16 v[62:65], v[152:155], v[196:199], v[62:65]
	v_mfma_f32_16x16x32_bf16 v[58:61], v[160:163], v[196:199], v[58:61]
	v_mfma_f32_16x16x32_bf16 v[50:53], v[152:155], v[204:207], v[50:53]
	v_mfma_f32_16x16x32_bf16 v[42:45], v[160:163], v[204:207], v[42:45]
	v_mfma_f32_16x16x32_bf16 v[34:37], v[152:155], v[212:215], v[34:37]
	v_mfma_f32_16x16x32_bf16 v[26:29], v[160:163], v[212:215], v[26:29]
	v_mfma_f32_16x16x32_bf16 v[18:21], v[152:155], v[220:223], v[18:21]
	v_mfma_f32_16x16x32_bf16 v[10:13], v[160:163], v[220:223], v[10:13]
	s_setprio 0
	s_setprio 1
	v_mfma_f32_16x16x32_bf16 v[54:57], v[176:179], v[192:195], v[54:57]
	v_mfma_f32_16x16x32_bf16 v[46:49], v[184:187], v[192:195], v[46:49]
	v_mfma_f32_16x16x32_bf16 v[38:41], v[176:179], v[200:203], v[38:41]
	v_mfma_f32_16x16x32_bf16 v[30:33], v[184:187], v[200:203], v[30:33]
	v_mfma_f32_16x16x32_bf16 v[22:25], v[176:179], v[208:211], v[22:25]
	v_mfma_f32_16x16x32_bf16 v[14:17], v[184:187], v[208:211], v[14:17]
	v_mfma_f32_16x16x32_bf16 v[6:9], v[176:179], v[216:219], v[6:9]
	v_mfma_f32_16x16x32_bf16 v[2:5], v[184:187], v[216:219], v[2:5]
	v_mfma_f32_16x16x32_bf16 v[54:57], v[180:183], v[196:199], v[54:57]
	v_mfma_f32_16x16x32_bf16 v[46:49], v[188:191], v[196:199], v[46:49]
	v_mfma_f32_16x16x32_bf16 v[38:41], v[180:183], v[204:207], v[38:41]
	v_mfma_f32_16x16x32_bf16 v[30:33], v[188:191], v[204:207], v[30:33]
	v_mfma_f32_16x16x32_bf16 v[22:25], v[180:183], v[212:215], v[22:25]
	v_mfma_f32_16x16x32_bf16 v[14:17], v[188:191], v[212:215], v[14:17]
	v_mfma_f32_16x16x32_bf16 v[6:9], v[180:183], v[220:223], v[6:9]
	v_mfma_f32_16x16x32_bf16 v[2:5], v[188:191], v[220:223], v[2:5]
	s_setprio 0
	s_barrier
	s_add_i32 s59, 0, 0x18000
	s_add_i32 s60, 0, 0x1c000
	v_add_u32_e32 v160, s59, v1
	v_add_u32_e32 v188, s60, v1
	ds_read_b128 v[148:151], v160
	ds_read_b128 v[152:155], v160 offset:1024
	ds_read_b128 v[156:159], v160 offset:2048
	ds_read_b128 v[160:163], v160 offset:3072
	ds_read_b128 v[176:179], v188
	ds_read_b128 v[180:183], v188 offset:1024
	ds_read_b128 v[184:187], v188 offset:2048
	ds_read_b128 v[188:191], v188 offset:3072
	s_add_u32 s26, s26, 0x40000
	s_addc_u32 s27, s27, 0
	s_mov_b32 m0, s34
	v_lshl_add_u64 v[232:233], s[26:27], 0, v[136:137]
	ds_read_b128 v[192:195], v172 offset:32768
	ds_read_b128 v[196:199], v172 offset:33792
	ds_read_b128 v[200:203], v172 offset:34816
	ds_read_b128 v[204:207], v172 offset:35840
	ds_read_b128 v[208:211], v172 offset:36864
	ds_read_b128 v[212:215], v172 offset:37888
	ds_read_b128 v[216:219], v172 offset:38912
	ds_read_b128 v[220:223], v172 offset:39936
	global_load_lds_dwordx4 v[232:233], off
	v_lshl_add_u64 v[232:233], s[26:27], 0, v[132:133]
	s_mov_b32 m0, s35
	s_nop 0
	global_load_lds_dwordx4 v[232:233], off
	s_waitcnt vmcnt(8)
	s_waitcnt lgkmcnt(0)
	s_barrier
	s_setprio 1
	s_waitcnt lgkmcnt(0)
	v_mfma_f32_16x16x32_bf16 v[126:129], v[148:151], v[192:195], v[126:129]
	v_mfma_f32_16x16x32_bf16 v[122:125], v[156:159], v[192:195], v[122:125]
	v_mfma_f32_16x16x32_bf16 v[114:117], v[148:151], v[200:203], v[114:117]
	v_mfma_f32_16x16x32_bf16 v[106:109], v[156:159], v[200:203], v[106:109]
	v_mfma_f32_16x16x32_bf16 v[98:101], v[148:151], v[208:211], v[98:101]
	v_mfma_f32_16x16x32_bf16 v[90:93], v[156:159], v[208:211], v[90:93]
	v_mfma_f32_16x16x32_bf16 v[82:85], v[148:151], v[216:219], v[82:85]
	v_mfma_f32_16x16x32_bf16 v[74:77], v[156:159], v[216:219], v[74:77]
	v_mfma_f32_16x16x32_bf16 v[126:129], v[152:155], v[196:199], v[126:129]
	v_mfma_f32_16x16x32_bf16 v[122:125], v[160:163], v[196:199], v[122:125]
	v_mfma_f32_16x16x32_bf16 v[114:117], v[152:155], v[204:207], v[114:117]
	v_mfma_f32_16x16x32_bf16 v[106:109], v[160:163], v[204:207], v[106:109]
	v_mfma_f32_16x16x32_bf16 v[98:101], v[152:155], v[212:215], v[98:101]
	v_mfma_f32_16x16x32_bf16 v[90:93], v[160:163], v[212:215], v[90:93]
	v_mfma_f32_16x16x32_bf16 v[82:85], v[152:155], v[220:223], v[82:85]
	v_mfma_f32_16x16x32_bf16 v[74:77], v[160:163], v[220:223], v[74:77]
	s_setprio 0
	s_setprio 1
	v_mfma_f32_16x16x32_bf16 v[118:121], v[176:179], v[192:195], v[118:121]
	v_mfma_f32_16x16x32_bf16 v[110:113], v[184:187], v[192:195], v[110:113]
	v_mfma_f32_16x16x32_bf16 v[102:105], v[176:179], v[200:203], v[102:105]
	v_mfma_f32_16x16x32_bf16 v[94:97], v[184:187], v[200:203], v[94:97]
	v_mfma_f32_16x16x32_bf16 v[86:89], v[176:179], v[208:211], v[86:89]
	v_mfma_f32_16x16x32_bf16 v[78:81], v[184:187], v[208:211], v[78:81]
	v_mfma_f32_16x16x32_bf16 v[70:73], v[176:179], v[216:219], v[70:73]
	v_mfma_f32_16x16x32_bf16 v[66:69], v[184:187], v[216:219], v[66:69]
	v_mfma_f32_16x16x32_bf16 v[118:121], v[180:183], v[196:199], v[118:121]
	v_mfma_f32_16x16x32_bf16 v[110:113], v[188:191], v[196:199], v[110:113]
	v_mfma_f32_16x16x32_bf16 v[102:105], v[180:183], v[204:207], v[102:105]
	v_mfma_f32_16x16x32_bf16 v[94:97], v[188:191], v[204:207], v[94:97]
	v_mfma_f32_16x16x32_bf16 v[86:89], v[180:183], v[212:215], v[86:89]
	v_mfma_f32_16x16x32_bf16 v[78:81], v[188:191], v[212:215], v[78:81]
	v_mfma_f32_16x16x32_bf16 v[70:73], v[180:183], v[220:223], v[70:73]
	v_mfma_f32_16x16x32_bf16 v[66:69], v[188:191], v[220:223], v[66:69]
	s_setprio 0
	s_barrier
; #define PG8_WAIT_V(n) asm volatile("s_waitcnt vmcnt(" #n ")" ::: "memory")
; #define PG8_BAR __builtin_amdgcn_s_barrier()
; __device__ __forceinline__ void rstd8(const float* SS, int rowb, int lane, float (&rs)[2][4]) {
;     f32x4 p[2][4];
; #pragma unroll
;     for (int ai = 0; ai < 2; ++ai)
; #pragma unroll
;         for (int m = 0; m < 4; ++m) p[ai][m] = *(const f32x4*)(SS + (size_t)(rowb + HALF * ai + 16 * m + (lane >> 2)) * 16 + 4 * (lane & 3));
;     asm volatile("" : "+v"(p[0][0]), "+v"(p[0][1]), "+v"(p[0][2]), "+v"(p[0][3]), "+v"(p[1][0]), "+v"(p[1][1]), "+v"(p[1][2]), "+v"(p[1][3]));
; template <class Epi, class Sched, bool ALIGN_EPI = false, bool SP2 = false>
; __device__ __forceinline__ void gemm_phase(PG8_LAS unsigned char* lds, const Gemm g, const Sched& S, const Epi& E, const bool skip_epi = false) {
;     ...
;             PG8_LDA(At, 1, 1); PG8_STAGE(PG8_SB(1, 0), b3, voffB); PG8_STAGE(PG8_SB(1, 1), b3 + hstep, voffB); PG8_STAGE_A(1, 0, a3, true);
;             PG8_WAIT_V(8); PG8_WAIT_L(0); PG8_BAR; PG8_MMA(1, 0, At, B0); PG8_MMA(1, 1, At, B1); PG8_BAR; PG8_SCHED;
;             } else {
;             PG8_LDB(B0, 0, 0); PG8_SCHED; PG8_LDA(At, 0, 0); PG8_STAGE_A(1, 1, a1, false);
;             PG8_WAIT_L(8); PG8_BAR; PG8_WAIT_L(0); PG8_MMA(0, 0, At, B0); PG8_BAR; PG8_SCHED;
;             PG8_LDB(B1, 0, 1); PG8_STAGE(PG8_SB(0, 0), b2, voffB);
;             PG8_BAR; PG8_WAIT_L(0); PG8_MMA(0, 1, At, B1); PG8_BAR;
;             PG8_LDA(At, 0, 1); PG8_STAGE_A(0, 0, a2, true);
;             PG8_BAR; PG8_WAIT_L(0); PG8_MMA(1, 0, At, B0); PG8_BAR; PG8_SCHED;
;             PG8_STAGE(PG8_SB(0, 1), b2 + hstep, voffB);
;             PG8_WAIT_V(6); PG8_BAR; PG8_MMA(1, 1, At, B1); PG8_BAR;
;             PG8_LDB(B0, 1, 0); PG8_SCHED; PG8_LDA(At, 1, 0); PG8_STAGE_A(0, 1, a2, true);
;             PG8_WAIT_L(8); PG8_BAR; PG8_WAIT_L(0); PG8_MMA(0, 0, At, B0); PG8_BAR; PG8_SCHED;
;             PG8_LDB(B1, 1, 1); PG8_STAGE(PG8_SB(1, 0), b3, voffB);
;             PG8_BAR; PG8_WAIT_L(0); PG8_MMA(0, 1, At, B1); PG8_BAR;
;             PG8_LDA(At, 1, 1); PG8_STAGE_A(1, 0, a3, true);
;             PG8_BAR; PG8_WAIT_L(0); PG8_MMA(1, 0, At, B0); PG8_BAR; PG8_SCHED;
;             PG8_STAGE(PG8_SB(1, 1), b3 + hstep, voffB);
;             PG8_WAIT_V(6); PG8_BAR; PG8_MMA(1, 1, At, B1); PG8_BAR;
;             }
;         }
;         if constexpr (ALIGN_EPI) { if (wr == 0) PG8_BAR; }
	s_add_i32 s26, s59, s28
	v_lshl_add_u64 v[164:165], v[164:165], 0, s[8:9]
	s_mov_b32 m0, s26
	ds_read_b128 v[192:195], v172 offset:49152
	ds_read_b128 v[196:199], v172 offset:50176
	ds_read_b128 v[200:203], v172 offset:51200
	ds_read_b128 v[204:207], v172 offset:52224
	ds_read_b128 v[208:211], v172 offset:53248
	ds_read_b128 v[212:215], v172 offset:54272
	ds_read_b128 v[216:219], v172 offset:55296
	ds_read_b128 v[220:223], v172 offset:56320
	global_load_lds_dwordx4 v[164:165], off
	s_add_i32 m0, s26, 0x2000
	s_add_u32 s24, s24, 0x40080
	v_lshl_add_u64 v[164:165], v[224:225], 0, s[8:9]
	s_addc_u32 s25, s25, 0
	s_add_i32 s26, s60, s28
	global_load_lds_dwordx4 v[164:165], off
	v_lshl_add_u64 v[164:165], s[24:25], 0, v[134:135]
	s_mov_b32 m0, s26
	s_nop 0
	global_load_lds_dwordx4 v[164:165], off
	v_lshl_add_u64 v[164:165], s[24:25], 0, v[130:131]
	s_add_i32 m0, s26, 0x2000
	s_nop 0
	global_load_lds_dwordx4 v[164:165], off
	v_lshl_add_u64 v[164:165], v[226:227], 0, s[8:9]
	s_mov_b32 m0, s37
	s_nop 0
	global_load_lds_dwordx4 v[164:165], off
	v_lshl_add_u64 v[164:165], v[230:231], 0, s[8:9]
	s_mov_b32 m0, s38
	s_nop 0
	global_load_lds_dwordx4 v[164:165], off
	s_waitcnt vmcnt(8)
	s_waitcnt lgkmcnt(0)
	s_barrier
	s_setprio 1
	s_waitcnt lgkmcnt(0)
	v_mfma_f32_16x16x32_bf16 v[62:65], v[148:151], v[192:195], v[62:65]
	v_mfma_f32_16x16x32_bf16 v[58:61], v[156:159], v[192:195], v[58:61]
	v_mfma_f32_16x16x32_bf16 v[50:53], v[148:151], v[200:203], v[50:53]
	v_mfma_f32_16x16x32_bf16 v[42:45], v[156:159], v[200:203], v[42:45]
	v_mfma_f32_16x16x32_bf16 v[34:37], v[148:151], v[208:211], v[34:37]
	v_mfma_f32_16x16x32_bf16 v[26:29], v[156:159], v[208:211], v[26:29]
	v_mfma_f32_16x16x32_bf16 v[18:21], v[148:151], v[216:219], v[18:21]
	v_mfma_f32_16x16x32_bf16 v[10:13], v[156:159], v[216:219], v[10:13]
	v_mfma_f32_16x16x32_bf16 v[62:65], v[152:155], v[196:199], v[62:65]
	v_mfma_f32_16x16x32_bf16 v[58:61], v[160:163], v[196:199], v[58:61]
	v_mfma_f32_16x16x32_bf16 v[50:53], v[152:155], v[204:207], v[50:53]
	v_mfma_f32_16x16x32_bf16 v[42:45], v[160:163], v[204:207], v[42:45]
	v_mfma_f32_16x16x32_bf16 v[34:37], v[152:155], v[212:215], v[34:37]
	v_mfma_f32_16x16x32_bf16 v[26:29], v[160:163], v[212:215], v[26:29]
	v_mfma_f32_16x16x32_bf16 v[18:21], v[152:155], v[220:223], v[18:21]
	v_mfma_f32_16x16x32_bf16 v[10:13], v[160:163], v[220:223], v[10:13]
	s_setprio 0
	s_setprio 1
	v_mfma_f32_16x16x32_bf16 v[54:57], v[176:179], v[192:195], v[54:57]
	v_mfma_f32_16x16x32_bf16 v[46:49], v[184:187], v[192:195], v[46:49]
	v_mfma_f32_16x16x32_bf16 v[38:41], v[176:179], v[200:203], v[38:41]
	v_mfma_f32_16x16x32_bf16 v[30:33], v[184:187], v[200:203], v[30:33]
	v_mfma_f32_16x16x32_bf16 v[22:25], v[176:179], v[208:211], v[22:25]
	v_mfma_f32_16x16x32_bf16 v[14:17], v[184:187], v[208:211], v[14:17]
	v_mfma_f32_16x16x32_bf16 v[6:9], v[176:179], v[216:219], v[6:9]
	v_mfma_f32_16x16x32_bf16 v[2:5], v[184:187], v[216:219], v[2:5]
	v_mfma_f32_16x16x32_bf16 v[54:57], v[180:183], v[196:199], v[54:57]
	v_mfma_f32_16x16x32_bf16 v[46:49], v[188:191], v[196:199], v[46:49]
	v_mfma_f32_16x16x32_bf16 v[38:41], v[180:183], v[204:207], v[38:41]
	v_mfma_f32_16x16x32_bf16 v[30:33], v[188:191], v[204:207], v[30:33]
	v_mfma_f32_16x16x32_bf16 v[22:25], v[180:183], v[212:215], v[22:25]
	v_mfma_f32_16x16x32_bf16 v[14:17], v[188:191], v[212:215], v[14:17]
	v_mfma_f32_16x16x32_bf16 v[6:9], v[180:183], v[220:223], v[6:9]
	v_mfma_f32_16x16x32_bf16 v[2:5], v[188:191], v[220:223], v[2:5]
	s_setprio 0
	s_barrier
	s_add_i32 s58, s58, 2
	s_add_u32 s22, s22, 0x100
	s_addc_u32 s23, s23, 0
	s_add_u32 s56, s56, 0x100
	s_addc_u32 s57, s57, 0
	s_cmp_gt_u32 s58, 13
	s_cbranch_scc0 .LBB0_944
	v_lshl_add_u32 v164, s20, 8, v167
	v_ashrrev_i32_e32 v165, 31, v164
	v_lshlrev_b64 v[148:149], 6, v[164:165]
	v_lshl_add_u64 v[148:149], v[138:139], 0, v[148:149]
	v_add_co_u32_e32 v150, vcc, 0x2000, v148
	v_addc_co_u32_e32 v151, vcc, 0, v149, vcc
	global_load_dwordx4 v[176:179], v[148:149], off
	global_load_dwordx4 v[180:183], v[148:149], off offset:1024
	global_load_dwordx4 v[184:187], v[148:149], off offset:2048
	global_load_dwordx4 v[188:191], v[148:149], off offset:3072
	global_load_dwordx4 v[192:195], v[150:151], off
	global_load_dwordx4 v[196:199], v[150:151], off offset:1024
	global_load_dwordx4 v[200:203], v[150:151], off offset:2048
	global_load_dwordx4 v[204:207], v[150:151], off offset:3072
	s_and_b64 vcc, exec, s[10:11]
	s_cbranch_vccz .LBB0_947
	s_barrier
; __device__ __forceinline__ unsigned cvt_pk_bf16(float lo, float hi) { const f32x2c_t v = {lo, hi}; return __builtin_bit_cast(unsigned, __builtin_convertvector(v, bf16x2c_t)); }
; __device__ __forceinline__ void rstd8(const float* SS, int rowb, int lane, float (&rs)[2][4]) {
;     f32x4 p[2][4];
; #pragma unroll
;     for (int ai = 0; ai < 2; ++ai)
; #pragma unroll
;         for (int m = 0; m < 4; ++m) p[ai][m] = *(const f32x4*)(SS + (size_t)(rowb + HALF * ai + 16 * m + (lane >> 2)) * 16 + 4 * (lane & 3));
;     asm volatile("" : "+v"(p[0][0]), "+v"(p[0][1]), "+v"(p[0][2]), "+v"(p[0][3]), "+v"(p[1][0]), "+v"(p[1][1]), "+v"(p[1][2]), "+v"(p[1][3]));
; #pragma unroll
;     for (int ai = 0; ai < 2; ++ai)
; #pragma unroll
;         for (int m = 0; m < 4; ++m) { float s = (p[ai][m][0] + p[ai][m][1]) + (p[ai][m][2] + p[ai][m][3]); s += __shfl_xor(s, 1); s += __shfl_xor(s, 2);
;             const float r = __builtin_amdgcn_rsqf(s * (1.0f / 1024.0f) + RMS_EPS);
;             rs[ai][m] = __builtin_bit_cast(float, __builtin_amdgcn_ds_bpermute((lane & 15) << 4, __builtin_bit_cast(int, r))); }
; }
;     __device__ __forceinline__ void operator()(const f32x4 (&acc)[2][2][4][2], const Unit& u, int wr, int wc, int fr, int fq) const {
;         const int row0 = u.pm * BM + wr * 64 + fr, col0 = u.pn * BM + wc * 32 + 8 * fq;
;         const float sc = (u.pn == 0) ? qs : ((u.pn == 3) ? 0.125f : 1.0f);
;         const int lane = fr + 16 * fq, qs4 = QSRC_ST(lane); const int rowS = u.pm * BM + wr * 64 + (lane >> 2), colS = u.pn * BM + wc * 32 + 8 * (lane & 3);
;         float rs8[2][4]; rstd8(SS, u.pm * BM + wr * 64, lane, rs8);
; #pragma unroll
;         for (int ai = 0; ai < 2; ++ai) {
; #pragma unroll
;             for (int m = 0; m < 4; ++m) { const float rs = rs8[ai][m] * sc;
;                 bf16_t* rowp = U + (size_t)(rowS + ai * HALF + m * 16) * ldu + colS;
; #pragma unroll
;                 for (int bj = 0; bj < 2; ++bj) { const f32x4 v0 = acc[ai][bj][m][0] * rs, v1 = acc[ai][bj][m][1] * rs;
;                     u32x4 w; w.x = cvt_pk_bf16(v0[0], v0[1]); w.y = cvt_pk_bf16(v0[2], v0[3]); w.z = cvt_pk_bf16(v1[0], v1[1]); w.w = cvt_pk_bf16(v1[2], v1[3]);
;                     *(u32x4*)(rowp + bj * HALF) = lane_perm(w, qs4); } } }
.LBB0_947:
	s_cmp_eq_u32 s53, 3
	s_cselect_b64 vcc, -1, 0
	v_cndmask_b32_e32 v156, 1.0, v174, vcc
	s_cmp_lg_u32 s53, 0
	s_cselect_b64 vcc, -1, 0
	v_cndmask_b32_e32 v156, v175, v156, vcc
	v_lshl_or_b32 v208, s53, 8, v169
	v_ashrrev_i32_e32 v209, 31, v208
	v_mov_b64_e32 v[154:155], s[44:45]
	v_lshlrev_b64 v[208:209], 1, v[208:209]
	v_mad_i64_i32 v[152:153], s[22:23], v164, s52, v[154:155]
	s_nop 0
	v_lshl_add_u64 v[208:209], v[152:153], 0, v[208:209]
	s_waitcnt vmcnt(0)
	v_add_f32_e32 v176, v176, v177
	v_add_f32_e32 v180, v180, v181
	v_add_f32_e32 v184, v184, v185
	v_add_f32_e32 v188, v188, v189
	v_add_f32_e32 v192, v192, v193
	v_add_f32_e32 v196, v196, v197
	v_add_f32_e32 v200, v200, v201
	v_add_f32_e32 v204, v204, v205
	v_add_f32_e32 v178, v178, v179
	v_add_f32_e32 v182, v182, v183
	v_add_f32_e32 v186, v186, v187
	v_add_f32_e32 v190, v190, v191
	v_add_f32_e32 v194, v194, v195
	v_add_f32_e32 v198, v198, v199
	v_add_f32_e32 v202, v202, v203
	v_add_f32_e32 v206, v206, v207
	v_add_f32_e32 v176, v176, v178
	v_add_f32_e32 v180, v180, v182
	v_add_f32_e32 v184, v184, v186
	v_add_f32_e32 v188, v188, v190
	v_add_f32_e32 v192, v192, v194
	v_add_f32_e32 v196, v196, v198
	v_add_f32_e32 v200, v200, v202
	v_add_f32_e32 v204, v204, v206
	v_add_f32_dpp v176, v176, v176 quad_perm:[1,0,3,2] row_mask:0xf bank_mask:0xf
	v_add_f32_dpp v180, v180, v180 quad_perm:[1,0,3,2] row_mask:0xf bank_mask:0xf
	v_add_f32_dpp v184, v184, v184 quad_perm:[1,0,3,2] row_mask:0xf bank_mask:0xf
	v_add_f32_dpp v188, v188, v188 quad_perm:[1,0,3,2] row_mask:0xf bank_mask:0xf
	v_add_f32_dpp v192, v192, v192 quad_perm:[1,0,3,2] row_mask:0xf bank_mask:0xf
	v_add_f32_dpp v196, v196, v196 quad_perm:[1,0,3,2] row_mask:0xf bank_mask:0xf
	v_add_f32_dpp v200, v200, v200 quad_perm:[1,0,3,2] row_mask:0xf bank_mask:0xf
	v_add_f32_dpp v204, v204, v204 quad_perm:[1,0,3,2] row_mask:0xf bank_mask:0xf
	v_add_f32_dpp v176, v176, v176 quad_perm:[2,3,0,1] row_mask:0xf bank_mask:0xf
	v_add_f32_dpp v180, v180, v180 quad_perm:[2,3,0,1] row_mask:0xf bank_mask:0xf
	v_add_f32_dpp v184, v184, v184 quad_perm:[2,3,0,1] row_mask:0xf bank_mask:0xf
	v_add_f32_dpp v188, v188, v188 quad_perm:[2,3,0,1] row_mask:0xf bank_mask:0xf
	v_add_f32_dpp v192, v192, v192 quad_perm:[2,3,0,1] row_mask:0xf bank_mask:0xf
	v_add_f32_dpp v196, v196, v196 quad_perm:[2,3,0,1] row_mask:0xf bank_mask:0xf
	v_add_f32_dpp v200, v200, v200 quad_perm:[2,3,0,1] row_mask:0xf bank_mask:0xf
	v_add_f32_dpp v204, v204, v204 quad_perm:[2,3,0,1] row_mask:0xf bank_mask:0xf
	v_fmamk_f32 v176, v176, 0x3a800000, v173
	v_fmamk_f32 v180, v180, 0x3a800000, v173
	v_fmamk_f32 v184, v184, 0x3a800000, v173
	v_fmamk_f32 v188, v188, 0x3a800000, v173
	v_fmamk_f32 v192, v192, 0x3a800000, v173
	v_fmamk_f32 v196, v196, 0x3a800000, v173
	v_fmamk_f32 v200, v200, 0x3a800000, v173
	v_fmamk_f32 v204, v204, 0x3a800000, v173
	ds_bpermute_b32 v176, v168, v176
	ds_bpermute_b32 v180, v168, v180
	ds_bpermute_b32 v184, v168, v184
	ds_bpermute_b32 v188, v168, v188
	ds_bpermute_b32 v192, v168, v192
	ds_bpermute_b32 v196, v168, v196
	ds_bpermute_b32 v200, v168, v200
	ds_bpermute_b32 v204, v168, v204
	s_waitcnt lgkmcnt(0)
	v_rsq_f32_e32 v178, v176
	v_rsq_f32_e32 v182, v180
	v_rsq_f32_e32 v186, v184
	v_rsq_f32_e32 v190, v188
	v_rsq_f32_e32 v194, v192
	v_rsq_f32_e32 v198, v196
	v_rsq_f32_e32 v202, v200
	v_rsq_f32_e32 v206, v204
	v_mul_f32_e32 v178, v156, v178
	v_mul_f32_e32 v182, v156, v182
	v_mul_f32_e32 v186, v156, v186
	v_mul_f32_e32 v190, v156, v190
	v_mul_f32_e32 v194, v156, v194
	v_mul_f32_e32 v198, v156, v198
	v_mul_f32_e32 v202, v156, v202
	v_mul_f32_e32 v206, v156, v206
	v_pk_mul_f32 v[126:127], v[126:127], v[178:179] op_sel_hi:[1,0]
	v_pk_mul_f32 v[128:129], v[128:129], v[178:179] op_sel_hi:[1,0]
	v_pk_mul_f32 v[122:123], v[122:123], v[178:179] op_sel_hi:[1,0]
	v_pk_mul_f32 v[124:125], v[124:125], v[178:179] op_sel_hi:[1,0]
	v_pk_mul_f32 v[118:119], v[118:119], v[178:179] op_sel_hi:[1,0]
	v_pk_mul_f32 v[120:121], v[120:121], v[178:179] op_sel_hi:[1,0]
	v_pk_mul_f32 v[110:111], v[110:111], v[178:179] op_sel_hi:[1,0]
	v_pk_mul_f32 v[112:113], v[112:113], v[178:179] op_sel_hi:[1,0]
	v_cvt_pk_bf16_f32 v126, v126, v127
	v_cvt_pk_bf16_f32 v127, v128, v129
	v_cvt_pk_bf16_f32 v128, v122, v123
	v_cvt_pk_bf16_f32 v129, v124, v125
	v_cvt_pk_bf16_f32 v118, v118, v119
	v_cvt_pk_bf16_f32 v119, v120, v121
	v_cvt_pk_bf16_f32 v120, v110, v111
	v_cvt_pk_bf16_f32 v121, v112, v113
	ds_bpermute_b32 v122, v166, v126
	ds_bpermute_b32 v123, v166, v127
	ds_bpermute_b32 v124, v166, v128
	ds_bpermute_b32 v125, v166, v129
	ds_bpermute_b32 v110, v166, v118
	ds_bpermute_b32 v111, v166, v119
	ds_bpermute_b32 v112, v166, v120
	ds_bpermute_b32 v113, v166, v121
	v_mov_b32_e32 v210, v208
	v_mov_b32_e32 v211, v209
	v_pk_mul_f32 v[114:115], v[114:115], v[182:183] op_sel_hi:[1,0]
	v_pk_mul_f32 v[116:117], v[116:117], v[182:183] op_sel_hi:[1,0]
	v_pk_mul_f32 v[106:107], v[106:107], v[182:183] op_sel_hi:[1,0]
	v_pk_mul_f32 v[108:109], v[108:109], v[182:183] op_sel_hi:[1,0]
	v_pk_mul_f32 v[102:103], v[102:103], v[182:183] op_sel_hi:[1,0]
	v_pk_mul_f32 v[104:105], v[104:105], v[182:183] op_sel_hi:[1,0]
	v_pk_mul_f32 v[94:95], v[94:95], v[182:183] op_sel_hi:[1,0]
	v_pk_mul_f32 v[96:97], v[96:97], v[182:183] op_sel_hi:[1,0]
	v_cvt_pk_bf16_f32 v114, v114, v115
	v_cvt_pk_bf16_f32 v115, v116, v117
	v_cvt_pk_bf16_f32 v116, v106, v107
	v_cvt_pk_bf16_f32 v117, v108, v109
	v_cvt_pk_bf16_f32 v102, v102, v103
	v_cvt_pk_bf16_f32 v103, v104, v105
	v_cvt_pk_bf16_f32 v104, v94, v95
	v_cvt_pk_bf16_f32 v105, v96, v97
	ds_bpermute_b32 v106, v166, v114
	ds_bpermute_b32 v107, v166, v115
	ds_bpermute_b32 v108, v166, v116
	ds_bpermute_b32 v109, v166, v117
	ds_bpermute_b32 v94, v166, v102
	ds_bpermute_b32 v95, v166, v103
	ds_bpermute_b32 v96, v166, v104
	ds_bpermute_b32 v97, v166, v105
	v_add_co_u32_e32 v212, vcc, 0x18000, v208
	v_addc_co_u32_e32 v213, vcc, 0, v209, vcc
	s_waitcnt lgkmcnt(8)
; __device__ __forceinline__ unsigned cvt_pk_bf16(float lo, float hi) { const f32x2c_t v = {lo, hi}; return __builtin_bit_cast(unsigned, __builtin_convertvector(v, bf16x2c_t)); }
;     __device__ __forceinline__ void operator()(const f32x4 (&acc)[2][2][4][2], const Unit& u, int wr, int wc, int fr, int fq) const {
;     ...
;         for (int ai = 0; ai < 2; ++ai) {
; #pragma unroll
;             for (int m = 0; m < 4; ++m) { const float rs = rs8[ai][m] * sc;
;                 bf16_t* rowp = U + (size_t)(rowS + ai * HALF + m * 16) * ldu + colS;
; #pragma unroll
;                 for (int bj = 0; bj < 2; ++bj) { const f32x4 v0 = acc[ai][bj][m][0] * rs, v1 = acc[ai][bj][m][1] * rs;
;                     u32x4 w; w.x = cvt_pk_bf16(v0[0], v0[1]); w.y = cvt_pk_bf16(v0[2], v0[3]); w.z = cvt_pk_bf16(v1[0], v1[1]); w.w = cvt_pk_bf16(v1[2], v1[3]);
;                     *(u32x4*)(rowp + bj * HALF) = lane_perm(w, qs4); } } }
	global_store_dwordx4 v[210:211], v[122:125], off
	global_store_dwordx4 v[210:211], v[110:113], off offset:256
	v_pk_mul_f32 v[98:99], v[98:99], v[186:187] op_sel_hi:[1,0]
	v_pk_mul_f32 v[100:101], v[100:101], v[186:187] op_sel_hi:[1,0]
	v_pk_mul_f32 v[90:91], v[90:91], v[186:187] op_sel_hi:[1,0]
	v_pk_mul_f32 v[92:93], v[92:93], v[186:187] op_sel_hi:[1,0]
	v_pk_mul_f32 v[86:87], v[86:87], v[186:187] op_sel_hi:[1,0]
	v_pk_mul_f32 v[88:89], v[88:89], v[186:187] op_sel_hi:[1,0]
	v_pk_mul_f32 v[78:79], v[78:79], v[186:187] op_sel_hi:[1,0]
	v_pk_mul_f32 v[80:81], v[80:81], v[186:187] op_sel_hi:[1,0]
	v_cvt_pk_bf16_f32 v98, v98, v99
	v_cvt_pk_bf16_f32 v99, v100, v101
	v_cvt_pk_bf16_f32 v100, v90, v91
	v_cvt_pk_bf16_f32 v101, v92, v93
	v_cvt_pk_bf16_f32 v86, v86, v87
	v_cvt_pk_bf16_f32 v87, v88, v89
	v_cvt_pk_bf16_f32 v88, v78, v79
	v_cvt_pk_bf16_f32 v89, v80, v81
	ds_bpermute_b32 v90, v166, v98
	ds_bpermute_b32 v91, v166, v99
	ds_bpermute_b32 v92, v166, v100
	ds_bpermute_b32 v93, v166, v101
	ds_bpermute_b32 v78, v166, v86
	ds_bpermute_b32 v79, v166, v87
	ds_bpermute_b32 v80, v166, v88
	ds_bpermute_b32 v81, v166, v89
	v_add_co_u32_e32 v210, vcc, 0x30000, v208
	v_addc_co_u32_e32 v211, vcc, 0, v209, vcc
	s_waitcnt lgkmcnt(8)
	global_store_dwordx4 v[212:213], v[106:109], off
	global_store_dwordx4 v[212:213], v[94:97], off offset:256
	v_pk_mul_f32 v[82:83], v[82:83], v[190:191] op_sel_hi:[1,0]
	v_pk_mul_f32 v[84:85], v[84:85], v[190:191] op_sel_hi:[1,0]
	v_pk_mul_f32 v[74:75], v[74:75], v[190:191] op_sel_hi:[1,0]
	v_pk_mul_f32 v[76:77], v[76:77], v[190:191] op_sel_hi:[1,0]
	v_pk_mul_f32 v[70:71], v[70:71], v[190:191] op_sel_hi:[1,0]
	v_pk_mul_f32 v[72:73], v[72:73], v[190:191] op_sel_hi:[1,0]
	v_pk_mul_f32 v[66:67], v[66:67], v[190:191] op_sel_hi:[1,0]
	v_pk_mul_f32 v[68:69], v[68:69], v[190:191] op_sel_hi:[1,0]
	v_cvt_pk_bf16_f32 v82, v82, v83
	v_cvt_pk_bf16_f32 v83, v84, v85
	v_cvt_pk_bf16_f32 v84, v74, v75
	v_cvt_pk_bf16_f32 v85, v76, v77
	v_cvt_pk_bf16_f32 v70, v70, v71
	v_cvt_pk_bf16_f32 v71, v72, v73
	v_cvt_pk_bf16_f32 v72, v66, v67
	v_cvt_pk_bf16_f32 v73, v68, v69
	ds_bpermute_b32 v74, v166, v82
	ds_bpermute_b32 v75, v166, v83
	ds_bpermute_b32 v76, v166, v84
	ds_bpermute_b32 v77, v166, v85
	ds_bpermute_b32 v66, v166, v70
	ds_bpermute_b32 v67, v166, v71
	ds_bpermute_b32 v68, v166, v72
	ds_bpermute_b32 v69, v166, v73
	v_add_co_u32_e32 v212, vcc, 0x48000, v208
	v_addc_co_u32_e32 v213, vcc, 0, v209, vcc
	s_waitcnt lgkmcnt(8)
	global_store_dwordx4 v[210:211], v[90:93], off
	global_store_dwordx4 v[210:211], v[78:81], off offset:256
	v_pk_mul_f32 v[62:63], v[62:63], v[194:195] op_sel_hi:[1,0]
	v_pk_mul_f32 v[64:65], v[64:65], v[194:195] op_sel_hi:[1,0]
	v_pk_mul_f32 v[58:59], v[58:59], v[194:195] op_sel_hi:[1,0]
	v_pk_mul_f32 v[60:61], v[60:61], v[194:195] op_sel_hi:[1,0]
	v_pk_mul_f32 v[54:55], v[54:55], v[194:195] op_sel_hi:[1,0]
	v_pk_mul_f32 v[56:57], v[56:57], v[194:195] op_sel_hi:[1,0]
	v_pk_mul_f32 v[46:47], v[46:47], v[194:195] op_sel_hi:[1,0]
	v_pk_mul_f32 v[48:49], v[48:49], v[194:195] op_sel_hi:[1,0]
	v_cvt_pk_bf16_f32 v62, v62, v63
	v_cvt_pk_bf16_f32 v63, v64, v65
	v_cvt_pk_bf16_f32 v64, v58, v59
	v_cvt_pk_bf16_f32 v65, v60, v61
	v_cvt_pk_bf16_f32 v54, v54, v55
	v_cvt_pk_bf16_f32 v55, v56, v57
	v_cvt_pk_bf16_f32 v56, v46, v47
	v_cvt_pk_bf16_f32 v57, v48, v49
	ds_bpermute_b32 v58, v166, v62
	ds_bpermute_b32 v59, v166, v63
	ds_bpermute_b32 v60, v166, v64
	ds_bpermute_b32 v61, v166, v65
	ds_bpermute_b32 v46, v166, v54
	ds_bpermute_b32 v47, v166, v55
	ds_bpermute_b32 v48, v166, v56
	ds_bpermute_b32 v49, v166, v57
	v_add_co_u32_e32 v210, vcc, 0xc0000, v208
	v_addc_co_u32_e32 v211, vcc, 0, v209, vcc
	s_waitcnt lgkmcnt(8)
; __device__ __forceinline__ unsigned cvt_pk_bf16(float lo, float hi) { const f32x2c_t v = {lo, hi}; return __builtin_bit_cast(unsigned, __builtin_convertvector(v, bf16x2c_t)); }
;     __device__ __forceinline__ void operator()(const f32x4 (&acc)[2][2][4][2], const Unit& u, int wr, int wc, int fr, int fq) const {
;     ...
;         for (int ai = 0; ai < 2; ++ai) {
; #pragma unroll
;             for (int m = 0; m < 4; ++m) { const float rs = rs8[ai][m] * sc;
;                 bf16_t* rowp = U + (size_t)(rowS + ai * HALF + m * 16) * ldu + colS;
; #pragma unroll
;                 for (int bj = 0; bj < 2; ++bj) { const f32x4 v0 = acc[ai][bj][m][0] * rs, v1 = acc[ai][bj][m][1] * rs;
;                     u32x4 w; w.x = cvt_pk_bf16(v0[0], v0[1]); w.y = cvt_pk_bf16(v0[2], v0[3]); w.z = cvt_pk_bf16(v1[0], v1[1]); w.w = cvt_pk_bf16(v1[2], v1[3]);
;                     *(u32x4*)(rowp + bj * HALF) = lane_perm(w, qs4); } } }
; template <class Epi, class Sched, bool ALIGN_EPI = false, bool SP2 = false>
; __device__ __forceinline__ void gemm_phase(PG8_LAS unsigned char* lds, const Gemm g, const Sched& S, const Epi& E, const bool skip_epi = false) {
;     ...
;         if (!has_next) break;
	global_store_dwordx4 v[212:213], v[74:77], off
	global_store_dwordx4 v[212:213], v[66:69], off offset:256
	v_pk_mul_f32 v[50:51], v[50:51], v[198:199] op_sel_hi:[1,0]
	v_pk_mul_f32 v[52:53], v[52:53], v[198:199] op_sel_hi:[1,0]
	v_pk_mul_f32 v[42:43], v[42:43], v[198:199] op_sel_hi:[1,0]
	v_pk_mul_f32 v[44:45], v[44:45], v[198:199] op_sel_hi:[1,0]
	v_pk_mul_f32 v[38:39], v[38:39], v[198:199] op_sel_hi:[1,0]
	v_pk_mul_f32 v[40:41], v[40:41], v[198:199] op_sel_hi:[1,0]
	v_pk_mul_f32 v[30:31], v[30:31], v[198:199] op_sel_hi:[1,0]
	v_pk_mul_f32 v[32:33], v[32:33], v[198:199] op_sel_hi:[1,0]
	v_cvt_pk_bf16_f32 v50, v50, v51
	v_cvt_pk_bf16_f32 v51, v52, v53
	v_cvt_pk_bf16_f32 v52, v42, v43
	v_cvt_pk_bf16_f32 v53, v44, v45
	v_cvt_pk_bf16_f32 v38, v38, v39
	v_cvt_pk_bf16_f32 v39, v40, v41
	v_cvt_pk_bf16_f32 v40, v30, v31
	v_cvt_pk_bf16_f32 v41, v32, v33
	ds_bpermute_b32 v42, v166, v50
	ds_bpermute_b32 v43, v166, v51
	ds_bpermute_b32 v44, v166, v52
	ds_bpermute_b32 v45, v166, v53
	ds_bpermute_b32 v30, v166, v38
	ds_bpermute_b32 v31, v166, v39
	ds_bpermute_b32 v32, v166, v40
	ds_bpermute_b32 v33, v166, v41
	v_add_co_u32_e32 v212, vcc, 0xd8000, v208
	v_addc_co_u32_e32 v213, vcc, 0, v209, vcc
	s_waitcnt lgkmcnt(8)
	global_store_dwordx4 v[210:211], v[58:61], off
	global_store_dwordx4 v[210:211], v[46:49], off offset:256
	v_pk_mul_f32 v[34:35], v[34:35], v[202:203] op_sel_hi:[1,0]
	v_pk_mul_f32 v[36:37], v[36:37], v[202:203] op_sel_hi:[1,0]
	v_pk_mul_f32 v[26:27], v[26:27], v[202:203] op_sel_hi:[1,0]
	v_pk_mul_f32 v[28:29], v[28:29], v[202:203] op_sel_hi:[1,0]
	v_pk_mul_f32 v[22:23], v[22:23], v[202:203] op_sel_hi:[1,0]
	v_pk_mul_f32 v[24:25], v[24:25], v[202:203] op_sel_hi:[1,0]
	v_pk_mul_f32 v[14:15], v[14:15], v[202:203] op_sel_hi:[1,0]
	v_pk_mul_f32 v[16:17], v[16:17], v[202:203] op_sel_hi:[1,0]
	v_cvt_pk_bf16_f32 v34, v34, v35
	v_cvt_pk_bf16_f32 v35, v36, v37
	v_cvt_pk_bf16_f32 v36, v26, v27
	v_cvt_pk_bf16_f32 v37, v28, v29
	v_cvt_pk_bf16_f32 v22, v22, v23
	v_cvt_pk_bf16_f32 v23, v24, v25
	v_cvt_pk_bf16_f32 v24, v14, v15
	v_cvt_pk_bf16_f32 v25, v16, v17
	ds_bpermute_b32 v26, v166, v34
	ds_bpermute_b32 v27, v166, v35
	ds_bpermute_b32 v28, v166, v36
	ds_bpermute_b32 v29, v166, v37
	ds_bpermute_b32 v14, v166, v22
	ds_bpermute_b32 v15, v166, v23
	ds_bpermute_b32 v16, v166, v24
	ds_bpermute_b32 v17, v166, v25
	v_add_co_u32_e32 v210, vcc, 0xf0000, v208
	v_addc_co_u32_e32 v211, vcc, 0, v209, vcc
	s_waitcnt lgkmcnt(8)
	global_store_dwordx4 v[212:213], v[42:45], off
	global_store_dwordx4 v[212:213], v[30:33], off offset:256
	v_pk_mul_f32 v[18:19], v[18:19], v[206:207] op_sel_hi:[1,0]
	v_pk_mul_f32 v[20:21], v[20:21], v[206:207] op_sel_hi:[1,0]
	v_pk_mul_f32 v[10:11], v[10:11], v[206:207] op_sel_hi:[1,0]
	v_pk_mul_f32 v[12:13], v[12:13], v[206:207] op_sel_hi:[1,0]
	v_pk_mul_f32 v[6:7], v[6:7], v[206:207] op_sel_hi:[1,0]
	v_pk_mul_f32 v[8:9], v[8:9], v[206:207] op_sel_hi:[1,0]
	v_pk_mul_f32 v[2:3], v[2:3], v[206:207] op_sel_hi:[1,0]
	v_pk_mul_f32 v[4:5], v[4:5], v[206:207] op_sel_hi:[1,0]
	v_cvt_pk_bf16_f32 v18, v18, v19
	v_cvt_pk_bf16_f32 v19, v20, v21
	v_cvt_pk_bf16_f32 v20, v10, v11
	v_cvt_pk_bf16_f32 v21, v12, v13
	v_cvt_pk_bf16_f32 v6, v6, v7
	v_cvt_pk_bf16_f32 v7, v8, v9
	v_cvt_pk_bf16_f32 v8, v2, v3
	v_cvt_pk_bf16_f32 v9, v4, v5
	ds_bpermute_b32 v10, v166, v18
	ds_bpermute_b32 v11, v166, v19
	ds_bpermute_b32 v12, v166, v20
	ds_bpermute_b32 v13, v166, v21
	ds_bpermute_b32 v2, v166, v6
	ds_bpermute_b32 v3, v166, v7
	ds_bpermute_b32 v4, v166, v8
	ds_bpermute_b32 v5, v166, v9
	v_add_co_u32_e32 v212, vcc, 0x108000, v208
	v_addc_co_u32_e32 v213, vcc, 0, v209, vcc
	s_waitcnt lgkmcnt(8)
	global_store_dwordx4 v[210:211], v[26:29], off
	global_store_dwordx4 v[210:211], v[14:17], off offset:256
	s_waitcnt lgkmcnt(0)
	global_store_dwordx4 v[212:213], v[10:13], off
	global_store_dwordx4 v[212:213], v[2:5], off offset:256
	s_andn2_b64 vcc, exec, s[4:5]
	s_mov_b64 s[4:5], -1
	s_cbranch_vccnz .LBB0_940
	s_andn2_b64 vcc, exec, s[6:7]
	s_cbranch_vccnz .LBB0_939
	s_barrier
	s_branch .LBB0_939
